# speedup vs baseline: 1.0325x; 1.0325x over previous
.LBB0_8:
	s_load_dwordx4 s[4:7], s[0:1], 0x0
	v_and_b32_e32 v1, 63, v0
	s_cmpk_gt_i32 s12, 0xff
	s_mov_b64 s[2:3], -1
	s_cbranch_scc0 .LBB0_24
	v_and_b32_e32 v74, 31, v0
	v_lshrrev_b32_e32 v75, 5, v1
	v_lshrrev_b32_e32 v76, 6, v0
	s_lshl_b32 s8, s12, 2
	s_cmpk_gt_u32 s12, 0x1ff
	v_mov_b32_e32 v39, 0
	v_add_u32_e32 v77, s8, v76
	v_lshlrev_b32_e32 v36, 2, v74
	v_lshlrev_b32_e32 v34, 17, v75
	s_cbranch_scc0 .LBB0_11
	v_add_u32_e32 v4, 0xfffff800, v77
	s_load_dwordx2 s[2:3], s[0:1], 0x30
	v_lshrrev_b32_e32 v2, 2, v4
	v_and_b32_e32 v38, 0x3fffffc0, v2
	v_lshlrev_b64 v[2:3], 14, v[38:39]
	v_lshlrev_b32_e32 v4, 6, v4
	v_bfe_u32 v78, v0, 6, 1
	s_waitcnt lgkmcnt(0)
	v_lshl_add_u64 v[2:3], s[6:7], 0, v[2:3]
	v_and_b32_e32 v40, 0x3f80, v4
	v_mov_b32_e32 v41, v39
	v_lshlrev_b32_e32 v4, 8, v74
	v_lshl_add_u64 v[2:3], v[2:3], 0, v[40:41]
	v_mov_b32_e32 v37, v39
	v_lshl_or_b32 v4, v78, 13, v4
	v_mov_b32_e32 v5, v39
	v_lshl_add_u64 v[2:3], v[2:3], 0, v[36:37]
	v_lshl_add_u64 v[4:5], s[2:3], 0, v[4:5]
	v_lshlrev_b32_e32 v6, 5, v75
	v_mov_b32_e32 v7, v39
	v_mov_b32_e32 v35, v39
	v_lshl_add_u64 v[42:43], v[4:5], 0, v[6:7]
	v_lshl_add_u64 v[44:45], v[2:3], 0, v[34:35]
	s_movk_i32 s2, 0x4000
	global_load_dwordx4 v[26:29], v[42:43], off offset:16
	global_load_dwordx4 v[30:33], v[42:43], off
	global_load_dwordx4 v[18:21], v[42:43], off offset:80
	global_load_dwordx4 v[22:25], v[42:43], off offset:64
	global_load_dwordx4 v[10:13], v[42:43], off offset:144
	global_load_dwordx4 v[14:17], v[42:43], off offset:128
	global_load_dwordx4 v[2:5], v[42:43], off offset:208
	global_load_dwordx4 v[6:9], v[42:43], off offset:192
	v_add_co_u32_e32 v42, vcc, s2, v44
	s_mov_b32 s3, 0x8000
	s_nop 0
	v_addc_co_u32_e32 v43, vcc, 0, v45, vcc
	v_add_co_u32_e32 v46, vcc, s3, v44
	s_mov_b32 s8, 0xc000
	s_nop 0
	v_addc_co_u32_e32 v47, vcc, 0, v45, vcc
	v_add_co_u32_e32 v48, vcc, s8, v44
	s_mov_b32 s9, 0x10000
	s_nop 0
	v_addc_co_u32_e32 v49, vcc, 0, v45, vcc
	v_add_co_u32_e32 v50, vcc, s9, v44
	s_mov_b32 s9, 0x14000
	s_nop 0
	v_addc_co_u32_e32 v51, vcc, 0, v45, vcc
	v_add_co_u32_e32 v52, vcc, s9, v44
	s_mov_b32 s9, 0x18000
	s_nop 0
	v_addc_co_u32_e32 v53, vcc, 0, v45, vcc
	v_add_co_u32_e32 v54, vcc, s9, v44
	s_mov_b32 s9, 0x1c000
	s_nop 0
	v_addc_co_u32_e32 v55, vcc, 0, v45, vcc
	v_add_co_u32_e32 v56, vcc, s9, v44
	s_mov_b32 s9, 0x40000
	s_nop 0
	v_addc_co_u32_e32 v57, vcc, 0, v45, vcc
	global_load_dword v72, v[44:45], off
	global_load_dword v73, v[42:43], off
	global_load_dword v70, v[46:47], off
	global_load_dword v71, v[48:49], off
	global_load_dword v68, v[50:51], off
	global_load_dword v69, v[52:53], off
	global_load_dword v66, v[54:55], off
	global_load_dword v67, v[56:57], off
	v_add_co_u32_e32 v42, vcc, s9, v44
	s_mov_b32 s10, 0x44000
	s_nop 0
	v_addc_co_u32_e32 v43, vcc, 0, v45, vcc
	v_add_co_u32_e32 v46, vcc, s10, v44
	s_mov_b32 s11, 0x48000
	s_nop 0
	v_addc_co_u32_e32 v47, vcc, 0, v45, vcc
	v_add_co_u32_e32 v48, vcc, s11, v44
	s_mov_b32 s13, 0x4c000
	s_nop 0
	v_addc_co_u32_e32 v49, vcc, 0, v45, vcc
	v_add_co_u32_e32 v50, vcc, s13, v44
	s_mov_b32 s14, 0x50000
	s_nop 0
	v_addc_co_u32_e32 v51, vcc, 0, v45, vcc
	v_add_co_u32_e32 v52, vcc, s14, v44
	s_mov_b32 s14, 0x54000
	s_nop 0
	v_addc_co_u32_e32 v53, vcc, 0, v45, vcc
	v_add_co_u32_e32 v54, vcc, s14, v44
	s_mov_b32 s14, 0x58000
	s_nop 0
	v_addc_co_u32_e32 v55, vcc, 0, v45, vcc
	v_add_co_u32_e32 v56, vcc, s14, v44
	s_mov_b32 s14, 0x5c000
	s_nop 0
	v_addc_co_u32_e32 v57, vcc, 0, v45, vcc
	v_add_co_u32_e32 v80, vcc, s14, v44
	s_mov_b32 s14, 0x80000
	s_nop 0
	v_addc_co_u32_e32 v81, vcc, 0, v45, vcc
	global_load_dword v64, v[42:43], off
	global_load_dword v65, v[46:47], off
	global_load_dword v62, v[48:49], off
	global_load_dword v63, v[50:51], off
	global_load_dword v60, v[52:53], off
	global_load_dword v61, v[54:55], off
	global_load_dword v58, v[56:57], off
	global_load_dword v59, v[80:81], off
	v_add_co_u32_e32 v42, vcc, s14, v44
	s_mov_b32 s14, 0x84000
	s_nop 0
	v_addc_co_u32_e32 v43, vcc, 0, v45, vcc
	v_add_co_u32_e32 v46, vcc, s14, v44
	s_mov_b32 s14, 0x88000
	s_nop 0
	v_addc_co_u32_e32 v47, vcc, 0, v45, vcc
	v_add_co_u32_e32 v48, vcc, s14, v44
	s_mov_b32 s14, 0x8c000
	s_nop 0
	v_addc_co_u32_e32 v49, vcc, 0, v45, vcc
	v_add_co_u32_e32 v54, vcc, s14, v44
	s_mov_b32 s14, 0x90000
	s_nop 0
	v_addc_co_u32_e32 v55, vcc, 0, v45, vcc
	v_add_co_u32_e32 v80, vcc, s14, v44
	s_mov_b32 s14, 0x94000
	s_nop 0
	v_addc_co_u32_e32 v81, vcc, 0, v45, vcc
	v_add_co_u32_e32 v82, vcc, s14, v44
	s_mov_b32 s14, 0x98000
	s_nop 0
	v_addc_co_u32_e32 v83, vcc, 0, v45, vcc
	global_load_dword v56, v[42:43], off
	global_load_dword v57, v[46:47], off
	global_load_dword v52, v[48:49], off
	global_load_dword v53, v[54:55], off
	global_load_dword v50, v[80:81], off
	global_load_dword v51, v[82:83], off
	v_add_co_u32_e32 v42, vcc, s14, v44
	s_mov_b32 s14, 0x9c000
	s_nop 0
	v_addc_co_u32_e32 v43, vcc, 0, v45, vcc
	v_add_co_u32_e32 v46, vcc, s14, v44
	s_mov_b32 s14, 0xc0000
	s_nop 0
	v_addc_co_u32_e32 v47, vcc, 0, v45, vcc
	global_load_dword v54, v[42:43], off
	global_load_dword v55, v[46:47], off
	v_add_co_u32_e32 v80, vcc, s14, v44
	s_mov_b32 s14, 0xc4000
	s_nop 0
	v_addc_co_u32_e32 v81, vcc, 0, v45, vcc
	v_add_co_u32_e32 v82, vcc, s14, v44
	s_mov_b32 s14, 0xc8000
	s_nop 0
	v_addc_co_u32_e32 v83, vcc, 0, v45, vcc
	v_add_co_u32_e32 v84, vcc, s14, v44
	s_mov_b32 s14, 0xcc000
	s_nop 0
	v_addc_co_u32_e32 v85, vcc, 0, v45, vcc
	v_add_co_u32_e32 v86, vcc, s14, v44
	s_mov_b32 s14, 0xd0000
	s_nop 0
	v_addc_co_u32_e32 v87, vcc, 0, v45, vcc
	v_add_co_u32_e32 v88, vcc, s14, v44
	s_mov_b32 s14, 0xd4000
	s_nop 0
	v_addc_co_u32_e32 v89, vcc, 0, v45, vcc
	v_add_co_u32_e32 v90, vcc, s14, v44
	s_mov_b32 s14, 0xd8000
	s_nop 0
	v_addc_co_u32_e32 v91, vcc, 0, v45, vcc
	v_add_co_u32_e32 v92, vcc, s14, v44
	s_mov_b32 s14, 0xdc000
	s_nop 0
	v_addc_co_u32_e32 v93, vcc, 0, v45, vcc
	v_add_co_u32_e32 v94, vcc, s14, v44
	s_load_dwordx2 s[14:15], s[0:1], 0x58
	s_nop 0
	v_addc_co_u32_e32 v95, vcc, 0, v45, vcc
	global_load_dword v48, v[80:81], off
	global_load_dword v49, v[82:83], off
	global_load_dword v46, v[84:85], off
	global_load_dword v47, v[86:87], off
	global_load_dword v44, v[88:89], off
	global_load_dword v45, v[90:91], off
	global_load_dword v42, v[92:93], off
	global_load_dword v43, v[94:95], off
	s_waitcnt vmcnt(38)
	s_waitcnt vmcnt(31)
	s_waitcnt vmcnt(30)
	s_waitcnt vmcnt(29)
	s_waitcnt vmcnt(28)
	s_waitcnt vmcnt(27)
	s_waitcnt vmcnt(26)
	s_waitcnt vmcnt(25)
	s_waitcnt vmcnt(24)
	s_waitcnt vmcnt(23)
	s_waitcnt vmcnt(22)
	s_waitcnt vmcnt(21)
	s_waitcnt vmcnt(20)
	s_waitcnt vmcnt(19)
	s_waitcnt vmcnt(18)
	s_waitcnt vmcnt(17)
	s_waitcnt vmcnt(16)
	v_cvt_pk_bf16_f32 v35, v72, 0
	v_cvt_pk_bf16_f32 v79, v73, 0
	v_lshlrev_b32_e32 v81, 16, v79
	v_lshlrev_b32_e32 v80, 16, v35
	v_pk_add_f32 v[82:83], v[72:73], v[80:81] neg_lo:[0,1] neg_hi:[0,1]
	v_cvt_pk_bf16_f32 v35, v70, 0
	v_cvt_pk_bf16_f32 v73, v71, 0
	v_lshlrev_b32_e32 v72, 16, v35
	v_lshlrev_b32_e32 v73, 16, v73
	v_pk_add_f32 v[84:85], v[70:71], v[72:73] neg_lo:[0,1] neg_hi:[0,1]
	v_cvt_pk_bf16_f32 v35, v68, 0
	v_cvt_pk_bf16_f32 v70, v69, 0
	v_lshlrev_b32_e32 v86, 16, v35
	v_lshlrev_b32_e32 v87, 16, v70
	v_pk_add_f32 v[88:89], v[68:69], v[86:87] neg_lo:[0,1] neg_hi:[0,1]
	v_cvt_pk_bf16_f32 v35, v66, 0
	v_cvt_pk_bf16_f32 v68, v67, 0
	v_lshlrev_b32_e32 v90, 16, v35
	v_lshlrev_b32_e32 v91, 16, v68
	v_pk_add_f32 v[92:93], v[66:67], v[90:91] neg_lo:[0,1] neg_hi:[0,1]
	v_cvt_pk_bf16_f32 v35, v30, 0
	v_cvt_pk_bf16_f32 v66, v31, 0
	v_cvt_pk_bf16_f32 v68, v26, 0
	v_lshlrev_b32_e32 v67, 16, v66
	v_lshlrev_b32_e32 v66, 16, v35
	v_cvt_pk_bf16_f32 v35, v27, 0
	v_lshlrev_b32_e32 v69, 16, v35
	v_lshlrev_b32_e32 v68, 16, v68
	v_pk_add_f32 v[94:95], v[26:27], v[68:69] neg_lo:[0,1] neg_hi:[0,1]
	v_cvt_pk_bf16_f32 v26, v32, 0
	v_cvt_pk_bf16_f32 v35, v28, 0
	v_cvt_pk_bf16_f32 v27, v33, 0
	v_cvt_pk_bf16_f32 v70, v29, 0
	v_lshlrev_b32_e32 v26, 16, v26
	v_lshlrev_b32_e32 v27, 16, v27
	v_lshlrev_b32_e32 v96, 16, v35
	v_lshlrev_b32_e32 v97, 16, v70
	v_pk_add_f32 v[30:31], v[30:31], v[66:67] neg_lo:[0,1] neg_hi:[0,1]
	v_cvt_pk_bf16_f32 v66, v66, v67
	v_cvt_pk_bf16_f32 v67, v26, v27
	v_cvt_pk_bf16_f32 v68, v68, v69
	v_cvt_pk_bf16_f32 v69, v96, v97
	v_cvt_pk_bf16_f32 v70, v80, v81
	v_cvt_pk_bf16_f32 v71, v72, v73
	v_cvt_pk_bf16_f32 v72, v86, v87
	v_cvt_pk_bf16_f32 v73, v90, v91
	v_pk_add_f32 v[32:33], v[32:33], v[26:27] neg_lo:[0,1] neg_hi:[0,1]
	v_pk_add_f32 v[80:81], v[28:29], v[96:97] neg_lo:[0,1] neg_hi:[0,1]
	v_mfma_f32_32x32x16_bf16 a[0:15], v[66:69], v[70:73], 0
	v_cvt_pk_bf16_f32 v26, v82, v83
	v_cvt_pk_bf16_f32 v27, v84, v85
	v_cvt_pk_bf16_f32 v28, v88, v89
	v_cvt_pk_bf16_f32 v29, v92, v93
	v_cvt_pk_bf16_f32 v30, v30, v31
	v_cvt_pk_bf16_f32 v31, v32, v33
	v_cvt_pk_bf16_f32 v32, v94, v95
	v_mfma_f32_32x32x16_bf16 a[0:15], v[66:69], v[26:29], a[0:15]
	v_cvt_pk_bf16_f32 v33, v80, v81
	v_cvt_pk_bf16_f32 v26, v64, 0
	v_cvt_pk_bf16_f32 v27, v65, 0
	v_cvt_pk_bf16_f32 v28, v18, 0
	v_cvt_pk_bf16_f32 v29, v19, 0
	v_lshlrev_b32_e32 v29, 16, v29
	v_lshlrev_b32_e32 v28, 16, v28
	v_mfma_f32_32x32x16_bf16 a[0:15], v[30:33], v[70:73], a[0:15]
	v_lshlrev_b32_e32 v30, 16, v26
	v_lshlrev_b32_e32 v31, 16, v27
	v_cvt_pk_bf16_f32 v26, v62, 0
	v_cvt_pk_bf16_f32 v27, v63, 0
	v_lshlrev_b32_e32 v32, 16, v26
	v_lshlrev_b32_e32 v33, 16, v27
	v_cvt_pk_bf16_f32 v26, v60, 0
	v_cvt_pk_bf16_f32 v27, v61, 0
	v_lshlrev_b32_e32 v66, 16, v26
	v_lshlrev_b32_e32 v67, 16, v27
	v_cvt_pk_bf16_f32 v26, v58, 0
	v_cvt_pk_bf16_f32 v27, v59, 0
	v_lshlrev_b32_e32 v68, 16, v26
	v_lshlrev_b32_e32 v69, 16, v27
	v_cvt_pk_bf16_f32 v26, v22, 0
	v_cvt_pk_bf16_f32 v27, v23, 0
	v_pk_add_f32 v[70:71], v[18:19], v[28:29] neg_lo:[0,1] neg_hi:[0,1]
	v_cvt_pk_bf16_f32 v18, v24, 0
	v_cvt_pk_bf16_f32 v35, v20, 0
	v_cvt_pk_bf16_f32 v19, v25, 0
	v_cvt_pk_bf16_f32 v73, v21, 0
	v_lshlrev_b32_e32 v27, 16, v27
	v_lshlrev_b32_e32 v26, 16, v26
	v_lshlrev_b32_e32 v18, 16, v18
	v_lshlrev_b32_e32 v19, 16, v19
	v_lshlrev_b32_e32 v72, 16, v35
	v_lshlrev_b32_e32 v73, 16, v73
	v_pk_add_f32 v[22:23], v[22:23], v[26:27] neg_lo:[0,1] neg_hi:[0,1]
	v_cvt_pk_bf16_f32 v26, v26, v27
	v_cvt_pk_bf16_f32 v27, v18, v19
	v_cvt_pk_bf16_f32 v28, v28, v29
	v_cvt_pk_bf16_f32 v29, v72, v73
	v_pk_add_f32 v[64:65], v[64:65], v[30:31] neg_lo:[0,1] neg_hi:[0,1]
	v_pk_add_f32 v[62:63], v[62:63], v[32:33] neg_lo:[0,1] neg_hi:[0,1]
	v_cvt_pk_bf16_f32 v30, v30, v31
	v_cvt_pk_bf16_f32 v31, v32, v33
	v_cvt_pk_bf16_f32 v32, v66, v67
	v_cvt_pk_bf16_f32 v33, v68, v69
	v_pk_add_f32 v[60:61], v[60:61], v[66:67] neg_lo:[0,1] neg_hi:[0,1]
	v_pk_add_f32 v[58:59], v[58:59], v[68:69] neg_lo:[0,1] neg_hi:[0,1]
	v_mfma_f32_32x32x16_bf16 a[0:15], v[26:29], v[30:33], a[0:15]
	v_add_f32_e64 v24, v24, -v18
	v_add_f32_e64 v25, v25, -v19
	v_add_f32_e64 v66, v20, -v72
	v_add_f32_e64 v67, v21, -v73
	v_cvt_pk_bf16_f32 v18, v64, v65
	v_cvt_pk_bf16_f32 v19, v62, v63
	v_cvt_pk_bf16_f32 v20, v60, v61
	v_cvt_pk_bf16_f32 v21, v58, v59
	v_cvt_pk_bf16_f32 v22, v22, v23
	v_cvt_pk_bf16_f32 v23, v24, v25
	v_mfma_f32_32x32x16_bf16 a[0:15], v[26:29], v[18:21], a[0:15]
	v_cvt_pk_bf16_f32 v24, v70, v71
	v_cvt_pk_bf16_f32 v25, v66, v67
	s_waitcnt vmcnt(15)
	s_waitcnt vmcnt(14)
	s_waitcnt vmcnt(13)
	s_waitcnt vmcnt(12)
	s_waitcnt vmcnt(11)
	s_waitcnt vmcnt(10)
	s_waitcnt vmcnt(9)
	s_waitcnt vmcnt(8)
	v_cvt_pk_bf16_f32 v20, v10, 0
	v_cvt_pk_bf16_f32 v18, v56, 0
	v_cvt_pk_bf16_f32 v19, v57, 0
	v_mfma_f32_32x32x16_bf16 a[0:15], v[22:25], v[30:33], a[0:15]
	v_lshlrev_b32_e32 v22, 16, v18
	v_lshlrev_b32_e32 v23, 16, v19
	v_cvt_pk_bf16_f32 v18, v52, 0
	v_cvt_pk_bf16_f32 v19, v53, 0
	v_lshlrev_b32_e32 v24, 16, v18
	v_lshlrev_b32_e32 v25, 16, v19
	v_cvt_pk_bf16_f32 v18, v50, 0
	v_cvt_pk_bf16_f32 v19, v51, 0
	v_lshlrev_b32_e32 v30, 16, v18
	v_lshlrev_b32_e32 v31, 16, v19
	v_cvt_pk_bf16_f32 v18, v54, 0
	v_cvt_pk_bf16_f32 v19, v55, 0
	v_cvt_pk_bf16_f32 v21, v11, 0
	v_pk_add_f32 v[32:33], v[50:51], v[30:31] neg_lo:[0,1] neg_hi:[0,1]
	v_lshlrev_b32_e32 v50, 16, v18
	v_lshlrev_b32_e32 v51, 16, v19
	v_lshlrev_b32_e32 v21, 16, v21
	v_lshlrev_b32_e32 v20, 16, v20
	v_pk_add_f32 v[26:27], v[56:57], v[22:23] neg_lo:[0,1] neg_hi:[0,1]
	v_pk_add_f32 v[28:29], v[52:53], v[24:25] neg_lo:[0,1] neg_hi:[0,1]
	v_pk_add_f32 v[52:53], v[54:55], v[50:51] neg_lo:[0,1] neg_hi:[0,1]
	v_cvt_pk_bf16_f32 v18, v14, 0
	v_cvt_pk_bf16_f32 v19, v15, 0
	v_pk_add_f32 v[54:55], v[10:11], v[20:21] neg_lo:[0,1] neg_hi:[0,1]
	v_cvt_pk_bf16_f32 v10, v16, 0
	v_cvt_pk_bf16_f32 v35, v12, 0
	v_cvt_pk_bf16_f32 v11, v17, 0
	v_cvt_pk_bf16_f32 v57, v13, 0
	v_lshlrev_b32_e32 v19, 16, v19
	v_lshlrev_b32_e32 v18, 16, v18
	v_lshlrev_b32_e32 v10, 16, v10
	v_lshlrev_b32_e32 v11, 16, v11
	v_lshlrev_b32_e32 v56, 16, v35
	v_lshlrev_b32_e32 v57, 16, v57
	v_pk_add_f32 v[14:15], v[14:15], v[18:19] neg_lo:[0,1] neg_hi:[0,1]
	v_cvt_pk_bf16_f32 v18, v18, v19
	v_cvt_pk_bf16_f32 v19, v10, v11
	v_cvt_pk_bf16_f32 v20, v20, v21
	v_cvt_pk_bf16_f32 v21, v56, v57
	v_cvt_pk_bf16_f32 v22, v22, v23
	v_cvt_pk_bf16_f32 v23, v24, v25
	v_cvt_pk_bf16_f32 v24, v30, v31
	v_cvt_pk_bf16_f32 v25, v50, v51
	v_pk_add_f32 v[16:17], v[16:17], v[10:11] neg_lo:[0,1] neg_hi:[0,1]
	v_pk_add_f32 v[30:31], v[12:13], v[56:57] neg_lo:[0,1] neg_hi:[0,1]
	v_mfma_f32_32x32x16_bf16 a[0:15], v[18:21], v[22:25], a[0:15]
	v_cvt_pk_bf16_f32 v10, v26, v27
	v_cvt_pk_bf16_f32 v11, v28, v29
	v_cvt_pk_bf16_f32 v12, v32, v33
	v_cvt_pk_bf16_f32 v13, v52, v53
	v_cvt_pk_bf16_f32 v14, v14, v15
	v_cvt_pk_bf16_f32 v15, v16, v17
	v_cvt_pk_bf16_f32 v16, v54, v55
	v_mfma_f32_32x32x16_bf16 a[0:15], v[18:21], v[10:13], a[0:15]
	v_cvt_pk_bf16_f32 v17, v30, v31
	s_waitcnt vmcnt(7)
	s_waitcnt vmcnt(6)
	s_waitcnt vmcnt(5)
	s_waitcnt vmcnt(4)
	s_waitcnt vmcnt(3)
	s_waitcnt vmcnt(2)
	s_waitcnt vmcnt(1)
	s_waitcnt vmcnt(0)
	v_lshl_or_b32 v38, v78, 5, v38
	v_cvt_pk_bf16_f32 v10, v48, 0
	v_cvt_pk_bf16_f32 v11, v49, 0
	v_mfma_f32_32x32x16_bf16 a[0:15], v[14:17], v[22:25], a[0:15]
	v_lshlrev_b32_e32 v14, 16, v10
	v_lshlrev_b32_e32 v15, 16, v11
	v_cvt_pk_bf16_f32 v10, v46, 0
	v_cvt_pk_bf16_f32 v11, v47, 0
	v_lshlrev_b32_e32 v16, 16, v10
	v_lshlrev_b32_e32 v17, 16, v11
	v_cvt_pk_bf16_f32 v10, v44, 0
	v_cvt_pk_bf16_f32 v11, v45, 0
	v_cvt_pk_bf16_f32 v12, v2, 0
	v_cvt_pk_bf16_f32 v13, v3, 0
	v_lshlrev_b32_e32 v22, 16, v10
	v_lshlrev_b32_e32 v23, 16, v11
	v_cvt_pk_bf16_f32 v10, v42, 0
	v_cvt_pk_bf16_f32 v11, v43, 0
	v_lshlrev_b32_e32 v13, 16, v13
	v_lshlrev_b32_e32 v12, 16, v12
	v_lshlrev_b32_e32 v26, 16, v10
	v_lshlrev_b32_e32 v27, 16, v11
	v_cvt_pk_bf16_f32 v10, v6, 0
	v_cvt_pk_bf16_f32 v11, v7, 0
	v_pk_add_f32 v[30:31], v[2:3], v[12:13] neg_lo:[0,1] neg_hi:[0,1]
	v_cvt_pk_bf16_f32 v2, v8, 0
	v_cvt_pk_bf16_f32 v32, v4, 0
	v_cvt_pk_bf16_f32 v3, v9, 0
	v_cvt_pk_bf16_f32 v33, v5, 0
	v_lshlrev_b32_e32 v11, 16, v11
	v_lshlrev_b32_e32 v10, 16, v10
	v_lshlrev_b32_e32 v2, 16, v2
	v_lshlrev_b32_e32 v3, 16, v3
	v_lshlrev_b32_e32 v32, 16, v32
	v_lshlrev_b32_e32 v33, 16, v33
	v_pk_add_f32 v[6:7], v[6:7], v[10:11] neg_lo:[0,1] neg_hi:[0,1]
	v_cvt_pk_bf16_f32 v10, v10, v11
	v_cvt_pk_bf16_f32 v11, v2, v3
	v_cvt_pk_bf16_f32 v12, v12, v13
	v_cvt_pk_bf16_f32 v13, v32, v33
	v_pk_add_f32 v[18:19], v[48:49], v[14:15] neg_lo:[0,1] neg_hi:[0,1]
	v_pk_add_f32 v[20:21], v[46:47], v[16:17] neg_lo:[0,1] neg_hi:[0,1]
	v_cvt_pk_bf16_f32 v14, v14, v15
	v_cvt_pk_bf16_f32 v15, v16, v17
	v_cvt_pk_bf16_f32 v16, v22, v23
	v_cvt_pk_bf16_f32 v17, v26, v27
	v_pk_add_f32 v[24:25], v[44:45], v[22:23] neg_lo:[0,1] neg_hi:[0,1]
	v_pk_add_f32 v[28:29], v[42:43], v[26:27] neg_lo:[0,1] neg_hi:[0,1]
	v_mfma_f32_32x32x16_bf16 a[0:15], v[10:13], v[14:17], a[0:15]
	v_add_f32_e64 v8, v8, -v2
	v_add_f32_e64 v9, v9, -v3
	v_add_f32_e64 v22, v4, -v32
	v_add_f32_e64 v23, v5, -v33
	v_cvt_pk_bf16_f32 v2, v18, v19
	v_cvt_pk_bf16_f32 v3, v20, v21
	v_cvt_pk_bf16_f32 v4, v24, v25
	v_cvt_pk_bf16_f32 v5, v28, v29
	v_cvt_pk_bf16_f32 v6, v6, v7
	v_cvt_pk_bf16_f32 v7, v8, v9
	v_mfma_f32_32x32x16_bf16 a[0:15], v[10:13], v[2:5], a[0:15]
	v_cvt_pk_bf16_f32 v8, v30, v31
	v_cvt_pk_bf16_f32 v9, v22, v23
	v_lshlrev_b64 v[2:3], 14, v[38:39]
	s_waitcnt lgkmcnt(0)
	v_lshl_add_u64 v[2:3], s[14:15], 0, v[2:3]
	v_lshl_add_u64 v[2:3], v[2:3], 0, v[40:41]
	v_lshl_add_u64 v[2:3], v[2:3], 0, v[36:37]
	v_lshlrev_b32_e32 v38, 16, v75
	v_mfma_f32_32x32x16_bf16 a[0:15], v[6:9], v[14:17], a[0:15]
	v_lshl_add_u64 v[2:3], v[2:3], 0, v[38:39]
	v_add_co_u32_e32 v4, vcc, s2, v2
	s_mov_b32 s2, 0x20000
	s_nop 0
	v_addc_co_u32_e32 v5, vcc, 0, v3, vcc
	s_nop 6
	global_store_dword v[4:5], a1, off sc1
	v_add_co_u32_e32 v4, vcc, s3, v2
	global_store_dword v[2:3], a0, off sc1
	s_nop 0
	v_addc_co_u32_e32 v5, vcc, 0, v3, vcc
	global_store_dword v[4:5], a2, off sc1
	v_add_co_u32_e32 v4, vcc, s8, v2
	s_nop 1
	v_addc_co_u32_e32 v5, vcc, 0, v3, vcc
	global_store_dword v[4:5], a3, off sc1
	v_add_co_u32_e32 v4, vcc, s2, v2
	s_mov_b32 s2, 0x24000
	s_nop 0
	v_addc_co_u32_e32 v5, vcc, 0, v3, vcc
	global_store_dword v[4:5], a4, off sc1
	v_add_co_u32_e32 v4, vcc, s2, v2
	s_mov_b32 s2, 0x28000
	s_nop 0
	v_addc_co_u32_e32 v5, vcc, 0, v3, vcc
	global_store_dword v[4:5], a5, off sc1
	v_add_co_u32_e32 v4, vcc, s2, v2
	s_mov_b32 s2, 0x2c000
	s_nop 0
	v_addc_co_u32_e32 v5, vcc, 0, v3, vcc
	global_store_dword v[4:5], a6, off sc1
	v_add_co_u32_e32 v4, vcc, s2, v2
	s_mov_b32 s2, 0x60000
	s_nop 0
	v_addc_co_u32_e32 v5, vcc, 0, v3, vcc
	global_store_dword v[4:5], a7, off sc1
	v_add_co_u32_e32 v4, vcc, s9, v2
	s_nop 1
	v_addc_co_u32_e32 v5, vcc, 0, v3, vcc
	global_store_dword v[4:5], a8, off sc1
	v_add_co_u32_e32 v4, vcc, s10, v2
	s_nop 1
	v_addc_co_u32_e32 v5, vcc, 0, v3, vcc
	global_store_dword v[4:5], a9, off sc1
	v_add_co_u32_e32 v4, vcc, s11, v2
	s_nop 1
	v_addc_co_u32_e32 v5, vcc, 0, v3, vcc
	global_store_dword v[4:5], a10, off sc1
	v_add_co_u32_e32 v4, vcc, s13, v2
	s_nop 1
	v_addc_co_u32_e32 v5, vcc, 0, v3, vcc
	global_store_dword v[4:5], a11, off sc1
	v_add_co_u32_e32 v4, vcc, s2, v2
	s_mov_b32 s2, 0x64000
	s_nop 0
	v_addc_co_u32_e32 v5, vcc, 0, v3, vcc
	global_store_dword v[4:5], a12, off sc1
	v_add_co_u32_e32 v4, vcc, s2, v2
	s_mov_b64 s[2:3], 0
	s_nop 0
	v_addc_co_u32_e32 v5, vcc, 0, v3, vcc
	global_store_dword v[4:5], a13, off sc1
	v_add_co_u32_e32 v4, vcc, 0x68000, v2
	s_nop 1
	v_addc_co_u32_e32 v5, vcc, 0, v3, vcc
	v_add_co_u32_e32 v2, vcc, 0x6c000, v2
	global_store_dword v[4:5], a14, off sc1
	s_nop 0
	v_addc_co_u32_e32 v3, vcc, 0, v3, vcc
	global_store_dword v[2:3], a15, off sc1

.LBB0_14:
	s_or_b64 exec, exec, s[10:11]
	v_lshlrev_b32_e32 v70, 3, v0
	v_and_b32_e32 v70, 0x78, v70
	v_or_b32_e32 v70, 0x2400, v70
	s_waitcnt vmcnt(1)
	v_cvt_pk_bf16_f32 v14, v14, v15
	v_cvt_pk_bf16_f32 v15, v16, v17
	v_lshrrev_b32_e32 v16, 4, v0
	s_movk_i32 s10, 0x90
	v_mad_u32_u24 v16, v16, s10, v70
	ds_write_b64 v16, v[14:15]
	v_or_b32_e32 v14, 0x100, v0
	v_cvt_pk_bf16_f32 v10, v10, v11
	v_cvt_pk_bf16_f32 v11, v12, v13
	v_lshrrev_b32_e32 v12, 4, v14
	v_mad_u32_u24 v12, v12, s10, v70
	ds_write_b64 v12, v[10:11]
	v_or_b32_e32 v10, 0x200, v0
	v_cvt_pk_bf16_f32 v6, v6, v7
	v_cvt_pk_bf16_f32 v7, v8, v9
	v_lshrrev_b32_e32 v8, 4, v10
	v_mad_u32_u24 v8, v8, s10, v70
	ds_write_b64 v8, v[6:7]
	v_or_b32_e32 v6, 0x300, v0
	s_waitcnt vmcnt(0)
	v_cvt_pk_bf16_f32 v2, v2, v3
	v_cvt_pk_bf16_f32 v3, v4, v5
	v_lshrrev_b32_e32 v4, 4, v6
	v_mad_u32_u24 v4, v4, s10, v70
	v_lshlrev_b32_e32 v6, 5, v76
	ds_write_b64 v4, v[2:3]
	v_cvt_pk_bf16_f32 v2, v26, v27
	v_cvt_pk_bf16_f32 v3, v28, v29
	v_cvt_pk_bf16_f32 v4, v34, v35
	v_cvt_pk_bf16_f32 v5, v36, v37
	v_mad_u32_u24 v6, v1, s10, v6
	v_lshlrev_b32_e32 v69, 5, v18
	ds_write_b128 v6, v[2:5]
	v_cvt_pk_bf16_f32 v2, v22, v23
	v_cvt_pk_bf16_f32 v3, v24, v25
	v_cvt_pk_bf16_f32 v4, v30, v31
	v_cvt_pk_bf16_f32 v5, v32, v33
	ds_write_b128 v6, v[2:5] offset:16
	s_and_saveexec_b64 s[2:3], vcc
	v_mov_b32_e32 v70, v21
	ds_write_b128 v20, v[70:73] offset:18432
	s_or_b64 exec, exec, s[2:3]
	v_lshlrev_b32_e32 v71, 4, v75
	v_mad_u32_u24 v75, v74, s10, v71
	s_waitcnt lgkmcnt(0)
	s_barrier
	ds_read_b128 v[2:5], v75 offset:9216
	ds_read_b128 v[10:13], v75 offset:9248
	v_cvt_pk_bf16_f32 v6, v44, v43
	v_cvt_pk_bf16_f32 v7, v42, v41
	v_cvt_pk_bf16_f32 v8, v40, v38
	v_cvt_pk_bf16_f32 v9, v19, v39
	s_mov_b32 s2, 0x3fb8aa3b
	v_cmp_gt_u32_e32 vcc, 32, v1
	s_waitcnt lgkmcnt(1)
	v_mfma_f32_32x32x16_bf16 a[16:31], v[2:5], v[6:9], 0
	ds_read_b128 v[2:5], v75 offset:13824
	ds_read_b128 v[14:17], v75 offset:13856
	ds_read_b128 v[20:23], v75 offset:9312
	s_waitcnt lgkmcnt(2)
	v_mfma_f32_32x32x16_bf16 a[0:15], v[2:5], v[6:9], 0
	v_cvt_pk_bf16_f32 v2, v52, v51
	v_cvt_pk_bf16_f32 v3, v50, v49
	v_cvt_pk_bf16_f32 v4, v48, v46
	v_cvt_pk_bf16_f32 v5, v45, v47
	ds_read_b128 v[6:9], v75 offset:9280
	s_nop 0
	v_mfma_f32_32x32x16_bf16 a[16:31], v[10:13], v[2:5], a[16:31]
	v_cvt_pk_bf16_f32 v10, v60, v59
	v_cvt_pk_bf16_f32 v11, v58, v57
	v_cvt_pk_bf16_f32 v12, v56, v54
	v_cvt_pk_bf16_f32 v13, v53, v55
	s_waitcnt lgkmcnt(0)
	s_nop 0
	v_mfma_f32_32x32x16_bf16 a[16:31], v[6:9], v[10:13], a[16:31]
	v_cvt_pk_bf16_f32 v6, v68, v67
	v_cvt_pk_bf16_f32 v7, v66, v65
	v_cvt_pk_bf16_f32 v8, v64, v62
	v_cvt_pk_bf16_f32 v9, v61, v63
	s_nop 1
	v_mfma_f32_32x32x16_bf16 a[16:31], v[20:23], v[6:9], a[16:31]
	ds_read_b128 v[20:23], v75 offset:13888
	v_mfma_f32_32x32x16_bf16 a[0:15], v[14:17], v[2:5], a[0:15]
	ds_read_b128 v[2:5], v75 offset:13920
	s_nop 8
	v_accvgpr_read_b32 v37, a19
	v_accvgpr_read_b32 v36, a18
	v_accvgpr_read_b32 v35, a21
	s_waitcnt lgkmcnt(1)
	v_mfma_f32_32x32x16_bf16 a[0:15], v[20:23], v[10:13], a[0:15]
	v_accvgpr_read_b32 v21, a17
	v_accvgpr_read_b32 v20, a16
	v_accvgpr_read_b32 v34, a20
	v_accvgpr_read_b32 v33, a23
	v_accvgpr_read_b32 v32, a22
	v_accvgpr_read_b32 v31, a25
	v_accvgpr_read_b32 v30, a24
	s_waitcnt lgkmcnt(0)
	v_mfma_f32_32x32x16_bf16 a[0:15], v[2:5], v[6:9], a[0:15]
	ds_read_b128 v[6:9], v71 offset:18432
	ds_read_b128 v[10:13], v71 offset:18688
	ds_read_b128 v[14:17], v71 offset:18464
	v_accvgpr_read_b32 v29, a27
	v_accvgpr_read_b32 v28, a26
	v_accvgpr_read_b32 v25, a31
	s_waitcnt lgkmcnt(2)
	v_pk_add_f32 v[84:85], v[6:7], v[20:21]
	ds_read_b128 v[20:23], v71 offset:18720
	s_waitcnt lgkmcnt(2)
	v_fma_f32 v70, v84, v10, 0
	v_pk_add_f32 v[36:37], v[8:9], v[36:37]
	v_fmac_f32_e32 v70, v85, v11
	v_fmac_f32_e32 v70, v36, v12
	ds_read_b128 v[6:9], v71 offset:18496
	v_fmac_f32_e32 v70, v37, v13
	s_waitcnt lgkmcnt(2)
	v_pk_add_f32 v[34:35], v[14:15], v[34:35]
	ds_read_b128 v[10:13], v71 offset:18752
	s_waitcnt lgkmcnt(2)
	v_fmac_f32_e32 v70, v34, v20
	v_fmac_f32_e32 v70, v35, v21
	v_pk_add_f32 v[32:33], v[16:17], v[32:33]
	ds_read_b128 v[14:17], v71 offset:18528
	v_fmac_f32_e32 v70, v32, v22
	v_fmac_f32_e32 v70, v33, v23
	s_waitcnt lgkmcnt(2)
	v_pk_add_f32 v[86:87], v[6:7], v[30:31]
	v_pk_add_f32 v[88:89], v[8:9], v[28:29]
	s_waitcnt lgkmcnt(1)
	v_fmac_f32_e32 v70, v86, v10
	v_fmac_f32_e32 v70, v87, v11
	v_accvgpr_read_b32 v24, a30
	v_accvgpr_read_b32 v27, a29
	v_accvgpr_read_b32 v26, a28
	v_fmac_f32_e32 v70, v88, v12
	ds_read_b128 v[6:9], v71 offset:18784
	v_fmac_f32_e32 v70, v89, v13
	s_waitcnt lgkmcnt(1)
	v_pk_add_f32 v[90:91], v[14:15], v[26:27]
	v_pk_add_f32 v[92:93], v[16:17], v[24:25]
	ds_read_b128 v[10:13], v71 offset:18560
	ds_read_b128 v[14:17], v71 offset:18816
	v_accvgpr_read_b32 v21, a1
	v_accvgpr_read_b32 v83, a3
	v_accvgpr_read_b32 v82, a2
	v_accvgpr_read_b32 v20, a0
	s_waitcnt lgkmcnt(1)
	v_pk_add_f32 v[94:95], v[10:11], v[20:21]
	v_pk_add_f32 v[82:83], v[12:13], v[82:83]
	ds_read_b128 v[10:13], v75
	v_fmac_f32_e32 v70, v90, v6
	v_fmac_f32_e32 v70, v91, v7
	v_fmac_f32_e32 v70, v92, v8
	v_fmac_f32_e32 v70, v93, v9
	ds_read_b128 v[6:9], v71 offset:18592
	ds_read_b128 v[20:23], v71 offset:18848
	s_waitcnt lgkmcnt(3)
	v_fmac_f32_e32 v70, v94, v14
	v_fmac_f32_e32 v70, v95, v15
	v_fmac_f32_e32 v70, v82, v16
	ds_read_b128 v[24:27], v75 offset:4608
	ds_read_b128 v[28:31], v75 offset:32
	v_accvgpr_read_b32 v81, a5
	v_accvgpr_read_b32 v80, a4
	v_fmac_f32_e32 v70, v83, v17
	v_cvt_pk_bf16_f32 v14, v84, v85
	v_cvt_pk_bf16_f32 v15, v36, v37
	v_cvt_pk_bf16_f32 v16, v34, v35
	v_cvt_pk_bf16_f32 v17, v32, v33
	v_accvgpr_read_b32 v79, a7
	v_accvgpr_read_b32 v78, a6
	s_waitcnt lgkmcnt(4)
	v_mfma_f32_32x32x16_bf16 a[16:31], v[10:13], v[14:17], 0
	s_waitcnt lgkmcnt(3)
	v_add_f32_e64 v32, v6, v80
	v_add_f32_e64 v33, v7, v81
	v_add_f32_e64 v34, v8, v78
	v_add_f32_e64 v35, v9, v79
	s_waitcnt lgkmcnt(2)
	v_fmac_f32_e32 v70, v32, v20
	ds_read_b128 v[6:9], v75 offset:4640
	ds_read_b128 v[10:13], v71 offset:18880
	v_accvgpr_read_b32 v3, a15
	v_accvgpr_read_b32 v2, a14
	v_accvgpr_read_b32 v5, a13
	v_accvgpr_read_b32 v4, a12
	v_accvgpr_read_b32 v73, a11
	v_accvgpr_read_b32 v72, a10
	v_accvgpr_read_b32 v77, a9
	v_accvgpr_read_b32 v76, a8
	v_fmac_f32_e32 v70, v33, v21
	s_waitcnt lgkmcnt(3)
	v_mfma_f32_32x32x16_bf16 a[0:15], v[24:27], v[14:17], 0
	v_fmac_f32_e32 v70, v34, v22
	v_fmac_f32_e32 v70, v35, v23
	ds_read_b128 v[20:23], v71 offset:18624
	ds_read_b128 v[24:27], v71 offset:18656
	v_cvt_pk_bf16_f32 v14, v86, v87
	v_cvt_pk_bf16_f32 v15, v88, v89
	v_cvt_pk_bf16_f32 v16, v90, v91
	v_cvt_pk_bf16_f32 v17, v92, v93
	s_waitcnt lgkmcnt(1)
	v_pk_add_f32 v[36:37], v[20:21], v[76:77]
	v_pk_add_f32 v[72:73], v[22:23], v[72:73]
	v_mfma_f32_32x32x16_bf16 a[16:31], v[28:31], v[14:17], a[16:31]
	ds_read_b128 v[28:31], v71 offset:18912
	ds_read_b128 v[20:23], v75 offset:64
	v_fmac_f32_e32 v70, v36, v10
	v_fmac_f32_e32 v70, v37, v11
	v_fmac_f32_e32 v70, v72, v12
	v_fmac_f32_e32 v70, v73, v13
	v_mov_b32_e32 v76, 0
	v_mfma_f32_32x32x16_bf16 a[0:15], v[6:9], v[14:17], a[0:15]
	ds_read_b128 v[10:13], v75 offset:4672
	ds_read_b128 v[14:17], v75 offset:96
	v_cvt_pk_bf16_f32 v6, v94, v95
	v_cvt_pk_bf16_f32 v7, v82, v83
	v_cvt_pk_bf16_f32 v8, v32, v33
	v_cvt_pk_bf16_f32 v9, v34, v35
	v_mov_b32_e32 v77, 0
	v_mov_b32_e32 v78, 0
	s_waitcnt lgkmcnt(2)
	v_mfma_f32_32x32x16_bf16 a[16:31], v[20:23], v[6:9], a[16:31]
	v_add_f32_e64 v20, v24, v4
	v_add_f32_e64 v21, v25, v5
	v_add_f32_e64 v22, v26, v2
	v_add_f32_e64 v23, v27, v3
	ds_read_b128 v[2:5], v75 offset:4704
	v_fmac_f32_e32 v70, v20, v28
	v_fmac_f32_e32 v70, v21, v29
	v_fmac_f32_e32 v70, v22, v30
	v_fmac_f32_e32 v70, v23, v31
	s_waitcnt lgkmcnt(2)
	v_mfma_f32_32x32x16_bf16 a[0:15], v[10:13], v[6:9], a[0:15]
	v_cvt_pk_bf16_f32 v6, v36, v37
	v_cvt_pk_bf16_f32 v7, v72, v73
	v_cvt_pk_bf16_f32 v8, v20, v21
	v_cvt_pk_bf16_f32 v9, v22, v23
	v_mov_b32_e32 v79, 0
	v_mov_b32_e32 v71, v70
	s_nop 1
	v_permlane32_swap_b32_e32 v70, v71
	s_waitcnt lgkmcnt(1)
	v_mfma_f32_32x32x16_bf16 a[16:31], v[14:17], v[6:9], a[16:31]
	s_waitcnt lgkmcnt(0)
	v_mfma_f32_32x32x16_bf16 a[0:15], v[2:5], v[6:9], a[0:15]
	s_nop 9
	v_accvgpr_read_b32 v25, a31
	v_accvgpr_read_b32 v24, a30
	v_accvgpr_read_b32 v2, a16
	v_accvgpr_read_b32 v15, a21
	v_accvgpr_read_b32 v14, a20
	v_accvgpr_read_b32 v13, a25
	v_accvgpr_read_b32 v12, a24
	v_accvgpr_read_b32 v23, a29
	v_accvgpr_read_b32 v37, a9
	v_accvgpr_read_b32 v36, a8
	v_accvgpr_read_b32 v22, a28
	v_pk_mul_f32 v[4:5], v[24:25], s[2:3] op_sel_hi:[1,0]
	v_accvgpr_read_b32 v3, a17
	v_pk_mul_f32 v[24:25], v[36:37], s[2:3] op_sel_hi:[1,0]
	v_accvgpr_read_b32 v37, a1
	v_accvgpr_read_b32 v11, a19
	v_accvgpr_read_b32 v10, a18
	v_accvgpr_read_b32 v33, a5
	v_accvgpr_read_b32 v32, a4
	v_accvgpr_read_b32 v81, a13
	v_accvgpr_read_b32 v80, a12
	v_accvgpr_read_b32 v83, a15
	v_accvgpr_read_b32 v82, a14
	v_pk_mul_f32 v[6:7], v[22:23], s[2:3] op_sel_hi:[1,0]
	v_pk_mul_f32 v[12:13], v[12:13], s[2:3] op_sel_hi:[1,0]
	v_pk_mul_f32 v[22:23], v[14:15], s[2:3] op_sel_hi:[1,0]
	v_pk_mul_f32 v[30:31], v[2:3], s[2:3] op_sel_hi:[1,0]
	v_mov_b32_e32 v3, 0
	v_accvgpr_read_b32 v36, a0
	v_pk_mul_f32 v[26:27], v[10:11], s[2:3] op_sel_hi:[1,0]
	v_cvt_pk_fp8_f32 v76, v30, v31
	v_cvt_pk_fp8_f32 v77, v22, v23
	v_cvt_pk_fp8_f32 v78, v12, v13
	v_cvt_pk_fp8_f32 v79, v6, v7
	v_pk_mul_f32 v[10:11], v[82:83], s[2:3] op_sel_hi:[1,0]
	v_pk_mul_f32 v[14:15], v[80:81], s[2:3] op_sel_hi:[1,0]
	v_pk_mul_f32 v[32:33], v[32:33], s[2:3] op_sel_hi:[1,0]
	v_pk_mul_f32 v[36:37], v[36:37], s[2:3] op_sel_hi:[1,0]
	v_mov_b32_e32 v80, v3
	v_mov_b32_e32 v81, v3
	v_mov_b32_e32 v82, v3
	v_mov_b32_e32 v83, v3
	v_cvt_pk_fp8_f32 v80, v36, v37
	v_cvt_pk_fp8_f32 v81, v32, v33
	v_cvt_pk_fp8_f32 v82, v24, v25
	v_cvt_pk_fp8_f32 v83, v14, v15
	v_accvgpr_read_b32 v17, a23
	v_accvgpr_read_b32 v16, a22
	v_accvgpr_read_b32 v21, a27
	v_accvgpr_read_b32 v20, a26
	v_accvgpr_read_b32 v35, a3
	v_accvgpr_read_b32 v34, a2
	v_accvgpr_read_b32 v29, a7
	v_accvgpr_read_b32 v28, a6
	v_accvgpr_read_b32 v73, a11
	v_accvgpr_read_b32 v72, a10
	v_pk_mul_f32 v[8:9], v[20:21], s[2:3] op_sel_hi:[1,0]
	v_pk_mul_f32 v[16:17], v[16:17], s[2:3] op_sel_hi:[1,0]
	v_cvt_pk_fp8_f32 v76, v26, v27 op_sel:[0,0,1]
	v_cvt_pk_fp8_f32 v77, v16, v17 op_sel:[0,0,1]
	v_cvt_pk_fp8_f32 v78, v8, v9 op_sel:[0,0,1]
	v_cvt_pk_fp8_f32 v79, v4, v5 op_sel:[0,0,1]
	v_pk_mul_f32 v[20:21], v[72:73], s[2:3] op_sel_hi:[1,0]
	v_pk_mul_f32 v[28:29], v[28:29], s[2:3] op_sel_hi:[1,0]
	v_pk_mul_f32 v[34:35], v[34:35], s[2:3] op_sel_hi:[1,0]
	v_cvt_pk_fp8_f32 v81, v28, v29 op_sel:[0,0,1]
	v_cvt_pk_fp8_f32 v80, v34, v35 op_sel:[0,0,1]
	v_cvt_pk_fp8_f32 v82, v20, v21 op_sel:[0,0,1]
	v_cvt_pk_fp8_f32 v83, v10, v11 op_sel:[0,0,1]
	v_lshl_or_b32 v2, v18, 7, v1
	v_lshl_add_u64 v[72:73], v[2:3], 4, s[8:9]
	v_or_b32_e32 v2, v69, v74
	global_store_dwordx4 v[72:73], v[76:79], off sc1
	global_store_dwordx4 v[72:73], v[80:83], off offset:1024 sc1
	s_and_saveexec_b64 s[2:3], vcc
	s_cbranch_execz .LBB0_18
	s_load_dwordx2 s[8:9], s[0:1], 0x50
	v_add_f32_e32 v69, v70, v71
	v_mul_f32_e32 v69, 0x3fb8aa3b, v69
	s_waitcnt lgkmcnt(0)
	v_lshl_add_u64 v[70:71], v[2:3], 2, s[8:9]
	global_store_dword v[70:71], v69, off sc1
.LBB0_18:
	s_or_b64 exec, exec, s[2:3]
	v_fma_f32 v44, v44, v44, 0
	v_fma_f32 v3, v30, v30, 0
	v_fmac_f32_e32 v44, v43, v43
	v_fmac_f32_e32 v3, v31, v31
	v_fmac_f32_e32 v44, v42, v42
	v_fmac_f32_e32 v3, v26, v26
	v_fmac_f32_e32 v44, v41, v41
	v_fmac_f32_e32 v3, v27, v27
	v_fmac_f32_e32 v44, v40, v40
	v_fmac_f32_e32 v3, v22, v22
	v_fmac_f32_e32 v44, v38, v38
	v_fmac_f32_e32 v3, v23, v23
	v_fmac_f32_e32 v44, v19, v19
	v_fmac_f32_e32 v3, v16, v16
	v_fmac_f32_e32 v44, v39, v39
	v_fmac_f32_e32 v3, v17, v17
	v_fmac_f32_e32 v44, v52, v52
	v_fmac_f32_e32 v3, v12, v12
	v_fmac_f32_e32 v44, v51, v51
	v_fmac_f32_e32 v3, v13, v13
	v_fmac_f32_e32 v44, v50, v50
	v_fmac_f32_e32 v3, v8, v8
	v_fmac_f32_e32 v44, v49, v49
	v_fmac_f32_e32 v3, v9, v9
	v_fmac_f32_e32 v44, v48, v48
	v_fmac_f32_e32 v3, v6, v6
	v_fmac_f32_e32 v44, v46, v46
	v_fmac_f32_e32 v3, v7, v7
	v_fmac_f32_e32 v44, v45, v45
	v_fmac_f32_e32 v3, v4, v4
	v_fmac_f32_e32 v44, v47, v47
	v_fmac_f32_e32 v3, v5, v5
	v_fmac_f32_e32 v44, v60, v60
	v_fmac_f32_e32 v3, v36, v36
	v_fmac_f32_e32 v44, v59, v59
	v_fmac_f32_e32 v3, v37, v37
	v_fmac_f32_e32 v44, v58, v58
	v_fmac_f32_e32 v3, v34, v34
	v_fmac_f32_e32 v44, v57, v57
	v_fmac_f32_e32 v3, v35, v35
	v_fmac_f32_e32 v44, v56, v56
	v_fmac_f32_e32 v3, v32, v32
	v_fmac_f32_e32 v44, v54, v54
	v_fmac_f32_e32 v3, v33, v33
	v_fmac_f32_e32 v44, v53, v53
	v_fmac_f32_e32 v3, v28, v28
	v_fmac_f32_e32 v44, v55, v55
	v_fmac_f32_e32 v3, v29, v29
	v_fmac_f32_e32 v44, v68, v68
	v_fmac_f32_e32 v3, v24, v24
	v_fmac_f32_e32 v44, v67, v67
	v_fmac_f32_e32 v3, v25, v25
	v_fmac_f32_e32 v44, v66, v66
	v_fmac_f32_e32 v3, v20, v20
	v_fmac_f32_e32 v44, v65, v65
	v_fmac_f32_e32 v3, v21, v21
	v_fmac_f32_e32 v44, v64, v64
	v_fmac_f32_e32 v3, v14, v14
	v_fmac_f32_e32 v44, v62, v62
	v_fmac_f32_e32 v3, v15, v15
	v_fmac_f32_e32 v44, v61, v61
	v_fmac_f32_e32 v3, v10, v10
	v_fmac_f32_e32 v44, v63, v63
	v_fmac_f32_e32 v3, v11, v11
	v_mov_b32_e32 v5, v3
	v_mov_b32_e32 v4, v44
	s_nop 0
	v_permlane32_swap_b32_e32 v3, v5
	v_permlane32_swap_b32_e32 v44, v4
	s_and_saveexec_b64 s[8:9], vcc
	s_cbranch_execz .LBB0_20
	v_add_f32_e32 v3, v3, v5
	s_mov_b32 s10, 0xf800000
	v_mul_f32_e32 v5, 0x4f800000, v3
	v_cmp_gt_f32_e32 vcc, s10, v3
	s_load_dwordx2 s[2:3], s[0:1], 0x60
	s_nop 0
	v_cndmask_b32_e32 v5, v3, v5, vcc
	v_sqrt_f32_e32 v6, v5
	v_mov_b32_e32 v3, 0
	s_waitcnt lgkmcnt(0)
	v_lshl_add_u64 v[2:3], v[2:3], 2, s[2:3]
	v_add_u32_e32 v7, -1, v6
	v_fma_f32 v8, -v7, v6, v5
	v_cmp_ge_f32_e64 s[2:3], 0, v8
	v_add_u32_e32 v8, 1, v6
	s_nop 0
	v_cndmask_b32_e64 v7, v6, v7, s[2:3]
	v_fma_f32 v6, -v8, v6, v5
	v_cmp_lt_f32_e64 s[2:3], 0, v6
	s_nop 1
	v_cndmask_b32_e64 v6, v7, v8, s[2:3]
	v_mul_f32_e32 v7, 0x37800000, v6
	v_cndmask_b32_e32 v6, v6, v7, vcc
	v_mov_b32_e32 v7, 0x260
	v_cmp_class_f32_e32 vcc, v5, v7
	s_nop 1
	v_cndmask_b32_e32 v5, v6, v5, vcc
	global_store_dword v[2:3], v5, off sc1
.LBB0_20:
	s_or_b64 exec, exec, s[8:9]
	v_mbcnt_lo_u32_b32 v3, -1, 0
	v_mbcnt_hi_u32_b32 v3, -1, v3
	v_add_f32_e32 v2, v44, v4
	v_and_b32_e32 v4, 64, v3
	v_add_u32_e32 v4, 64, v4
	v_xor_b32_e32 v5, 16, v3
	v_cmp_lt_i32_e32 vcc, v5, v4
	v_xor_b32_e32 v6, 8, v3
	s_nop 0
	v_cndmask_b32_e32 v5, v3, v5, vcc
	v_lshlrev_b32_e32 v5, 2, v5
	ds_bpermute_b32 v5, v5, v2
	v_cmp_lt_i32_e32 vcc, v6, v4
	s_waitcnt lgkmcnt(0)
	v_max_f32_e32 v5, v5, v5
	v_max_f32_e32 v2, v2, v5
	v_cndmask_b32_e32 v5, v3, v6, vcc
	v_lshlrev_b32_e32 v5, 2, v5
	ds_bpermute_b32 v5, v5, v2
	v_xor_b32_e32 v6, 4, v3
	v_cmp_lt_i32_e32 vcc, v6, v4
	s_waitcnt lgkmcnt(0)
	v_max_f32_e32 v5, v5, v5
	v_max_f32_e32 v2, v2, v5
	v_cndmask_b32_e32 v5, v3, v6, vcc
	v_lshlrev_b32_e32 v5, 2, v5
	ds_bpermute_b32 v5, v5, v2
	v_xor_b32_e32 v6, 2, v3
	v_cmp_lt_i32_e32 vcc, v6, v4
	s_waitcnt lgkmcnt(0)
	v_max_f32_e32 v5, v5, v5
	v_max_f32_e32 v2, v2, v5
	v_cndmask_b32_e32 v5, v3, v6, vcc
	v_lshlrev_b32_e32 v5, 2, v5
	ds_bpermute_b32 v5, v5, v2
	v_xor_b32_e32 v6, 1, v3
	v_cmp_lt_i32_e32 vcc, v6, v4
	s_waitcnt lgkmcnt(0)
	v_max_f32_e32 v5, v5, v5
	v_cndmask_b32_e32 v3, v3, v6, vcc
	v_max_f32_e32 v2, v2, v5
	v_lshlrev_b32_e32 v3, 2, v3
	ds_bpermute_b32 v3, v3, v2
	v_cmp_eq_u32_e32 vcc, 0, v1
	s_and_saveexec_b64 s[2:3], vcc
	s_cbranch_execz .LBB0_22
	s_load_dwordx2 s[8:9], s[0:1], 0x68
	s_waitcnt lgkmcnt(0)
	v_max_f32_e32 v3, v3, v3
	v_max_f32_e32 v2, v2, v2
	v_mov_b32_e32 v19, 0
	v_max_f32_e32 v4, v2, v3
	v_lshl_add_u64 v[2:3], v[18:19], 2, s[8:9]
	global_store_dword v[2:3], v4, off sc1

.LBB0_24:
	s_andn2_b64 vcc, exec, s[2:3]
	s_cbranch_vccnz .LBB0_29
	v_lshl_or_b32 v2, s12, 8, v0
	s_movk_i32 s2, 0x7fff
	v_cmp_lt_i32_e32 vcc, s2, v2
	s_and_saveexec_b64 s[2:3], vcc
	s_xor_b64 s[2:3], exec, s[2:3]
	s_cbranch_execz .LBB0_27
	v_add_u32_e32 v22, 0xffff8000, v2
	v_lshrrev_b32_e32 v1, 8, v22
	v_and_b32_e32 v4, 0xffffc0, v1
	v_mov_b32_e32 v5, 0
	v_lshlrev_b64 v[6:7], 14, v[4:5]
	v_lshlrev_b32_e32 v1, 14, v0
	s_waitcnt lgkmcnt(0)
	v_lshl_add_u64 v[6:7], s[6:7], 0, v[6:7]
	v_and_b32_e32 v4, 0xfc000, v1
	v_lshl_add_u64 v[6:7], v[6:7], 0, v[4:5]
	v_and_b32_e32 v4, 0x3f00, v2
	v_lshlrev_b32_e32 v1, 1, v0
	v_lshl_add_u64 v[2:3], v[6:7], 0, v[4:5]
	v_and_b32_e32 v4, 0x80, v1
	v_lshrrev_b32_e32 v0, 3, v0
	v_lshl_add_u64 v[2:3], v[2:3], 0, v[4:5]
	v_and_b32_e32 v4, 16, v0
	v_lshl_add_u64 v[0:1], v[2:3], 0, v[4:5]
	global_load_dwordx4 v[6:9], v[0:1], off
	global_load_dwordx4 v[10:13], v[0:1], off offset:32
	global_load_dwordx4 v[14:17], v[0:1], off offset:64
	global_load_dwordx4 v[18:21], v[0:1], off offset:96
	v_mov_b32_e32 v2, v5
	v_mov_b32_e32 v3, v5
	v_mov_b32_e32 v4, v5
	v_mov_b32_e32 v23, v5
	s_load_dwordx2 s[6:7], s[0:1], 0x40
	s_waitcnt lgkmcnt(0)
	v_lshl_add_u64 v[0:1], v[22:23], 4, s[6:7]
	s_waitcnt vmcnt(3)
	v_cvt_pk_fp8_f32 v2, v6, v7
	s_waitcnt vmcnt(2)
	v_cvt_pk_fp8_f32 v3, v10, v11
	s_waitcnt vmcnt(1)
	v_cvt_pk_fp8_f32 v4, v14, v15
	s_waitcnt vmcnt(0)
	v_cvt_pk_fp8_f32 v5, v18, v19
	v_cvt_pk_fp8_f32 v2, v8, v9 op_sel:[0,0,1]
	v_cvt_pk_fp8_f32 v3, v12, v13 op_sel:[0,0,1]
	v_cvt_pk_fp8_f32 v4, v16, v17 op_sel:[0,0,1]
	v_cvt_pk_fp8_f32 v5, v20, v21 op_sel:[0,0,1]
	global_store_dwordx4 v[0:1], v[2:5], off sc1
.LBB0_27:
	s_andn2_saveexec_b64 s[2:3], s[2:3]
	s_cbranch_execz .LBB0_29
	v_ashrrev_i32_e32 v4, 14, v2
	s_waitcnt lgkmcnt(0)
	v_lshrrev_b32_e32 v3, 1, v0
	v_lshrrev_b32_e32 v0, 5, v0
	v_ashrrev_i32_e32 v5, 31, v4
	v_and_b32_e32 v0, 4, v0
	v_lshlrev_b64 v[4:5], 20, v[4:5]
	v_and_or_b32 v0, v3, 32, v0
	v_lshl_add_u64 v[4:5], s[4:5], 0, v[4:5]
	v_lshlrev_b32_e32 v6, 14, v0
	v_mov_b32_e32 v7, 0
	v_lshl_add_u64 v[4:5], v[4:5], 0, v[6:7]
	v_and_b32_e32 v6, 0x3f00, v2
	v_lshl_add_u64 v[4:5], v[4:5], 0, v[6:7]
	v_lshlrev_b32_e32 v6, 2, v1
	v_lshl_add_u64 v[0:1], v[4:5], 0, v[6:7]
	s_movk_i32 s2, 0x4000
	v_add_co_u32_e32 v4, vcc, s2, v0
	s_mov_b32 s2, 0x8000
	s_nop 0
	v_addc_co_u32_e32 v5, vcc, 0, v1, vcc
	v_add_co_u32_e32 v8, vcc, s2, v0
	s_mov_b32 s2, 0xc000
	s_nop 0
	v_addc_co_u32_e32 v9, vcc, 0, v1, vcc
	v_add_co_u32_e32 v10, vcc, s2, v0
	s_mov_b32 s2, 0x20000
	s_nop 0
	v_addc_co_u32_e32 v11, vcc, 0, v1, vcc
	v_add_co_u32_e32 v12, vcc, s2, v0
	s_mov_b32 s2, 0x24000
	s_nop 0
	v_addc_co_u32_e32 v13, vcc, 0, v1, vcc
	v_add_co_u32_e32 v14, vcc, s2, v0
	s_mov_b32 s2, 0x28000
	s_nop 0
	v_addc_co_u32_e32 v15, vcc, 0, v1, vcc
	v_add_co_u32_e32 v16, vcc, s2, v0
	s_mov_b32 s2, 0x2c000
	s_nop 0
	v_addc_co_u32_e32 v17, vcc, 0, v1, vcc
	v_add_co_u32_e32 v18, vcc, s2, v0
	s_mov_b32 s2, 0x40000
	s_nop 0
	v_addc_co_u32_e32 v19, vcc, 0, v1, vcc
	global_load_dword v3, v[0:1], off
	global_load_dword v6, v[4:5], off
	global_load_dword v20, v[8:9], off
	global_load_dword v21, v[10:11], off
	global_load_dword v22, v[12:13], off
	global_load_dword v23, v[14:15], off
	global_load_dword v24, v[16:17], off
	global_load_dword v25, v[18:19], off
	v_add_co_u32_e32 v4, vcc, s2, v0
	s_mov_b32 s2, 0x44000
	s_nop 0
	v_addc_co_u32_e32 v5, vcc, 0, v1, vcc
	v_add_co_u32_e32 v8, vcc, s2, v0
	s_mov_b32 s2, 0x48000
	s_nop 0
	v_addc_co_u32_e32 v9, vcc, 0, v1, vcc
	v_add_co_u32_e32 v10, vcc, s2, v0
	s_mov_b32 s2, 0x4c000
	s_nop 0
	v_addc_co_u32_e32 v11, vcc, 0, v1, vcc
	v_add_co_u32_e32 v12, vcc, s2, v0
	s_mov_b32 s2, 0x60000
	s_nop 0
	v_addc_co_u32_e32 v13, vcc, 0, v1, vcc
	v_add_co_u32_e32 v14, vcc, s2, v0
	s_mov_b32 s2, 0x64000
	s_nop 0
	v_addc_co_u32_e32 v15, vcc, 0, v1, vcc
	v_add_co_u32_e32 v16, vcc, s2, v0
	s_mov_b32 s2, 0x68000
	s_nop 0
	v_addc_co_u32_e32 v17, vcc, 0, v1, vcc
	v_add_co_u32_e32 v18, vcc, s2, v0
	s_mov_b32 s2, 0x6c000
	s_nop 0
	v_addc_co_u32_e32 v19, vcc, 0, v1, vcc
	v_add_co_u32_e32 v0, vcc, s2, v0
	s_load_dwordx2 s[0:1], s[0:1], 0x38
	s_nop 0
	v_addc_co_u32_e32 v1, vcc, 0, v1, vcc
	global_load_dword v26, v[4:5], off
	global_load_dword v27, v[8:9], off
	global_load_dword v28, v[14:15], off
	global_load_dword v29, v[16:17], off
	global_load_dword v30, v[10:11], off
	global_load_dword v31, v[12:13], off
	global_load_dword v32, v[18:19], off
	global_load_dword v33, v[0:1], off
	v_mov_b32_e32 v4, v7
	v_mov_b32_e32 v5, v7
	s_waitcnt vmcnt(14)
	v_cvt_pk_fp8_f32 v4, v3, v6
	v_mov_b32_e32 v6, v7
	v_ashrrev_i32_e32 v3, 31, v2
	s_waitcnt lgkmcnt(0)
	v_lshl_add_u64 v[0:1], v[2:3], 4, s[0:1]
	s_waitcnt vmcnt(10)
	v_cvt_pk_fp8_f32 v5, v22, v23
	v_cvt_pk_fp8_f32 v4, v20, v21 op_sel:[0,0,1]
	s_waitcnt vmcnt(8)
	v_cvt_pk_fp8_f32 v5, v24, v25 op_sel:[0,0,1]
	s_waitcnt vmcnt(6)
	v_cvt_pk_fp8_f32 v6, v26, v27
	s_waitcnt vmcnt(4)
	v_cvt_pk_fp8_f32 v7, v28, v29
	s_waitcnt vmcnt(2)
	v_cvt_pk_fp8_f32 v6, v30, v31 op_sel:[0,0,1]
	s_waitcnt vmcnt(0)
	v_cvt_pk_fp8_f32 v7, v32, v33 op_sel:[0,0,1]
	global_store_dwordx4 v[0:1], v[4:7], off sc1

_Z11attn_kernelPKfS0_S0_PKcS2_PKDv4_jS0_S0_S0_S0_Pf:
	s_load_dwordx8 s[4:11], s[0:1], 0x0
	s_load_dwordx8 s[12:19], s[0:1], 0x20
	v_readfirstlane_b32 s20, v0
	s_bfe_u32 s28, s2, 0x10002
	s_lshr_b32 s29, s20, 6
	s_lshr_b32 s3, s20, 8
	s_bfe_u32 s30, s20, 0x20006
	s_lshr_b32 s31, s2, 3
	s_lshl_b32 s24, s28, 18
	s_waitcnt lgkmcnt(0)
	s_add_u32 s20, s10, s24
	s_addc_u32 s10, s11, 0
	s_and_b32 s21, s10, 0xffff
	s_add_u32 s24, s12, s24
	s_addc_u32 s10, s13, 0
	v_and_b32_e32 v1, 63, v0
	s_and_b32 s25, s10, 0xffff
	s_lshl_b32 s10, s30, 10
	s_lshl_b32 s38, s3, 12
	v_lshlrev_b32_e32 v2, 4, v1
	s_or_b32 s35, s10, s38
	v_lshl_or_b32 v2, s3, 17, v2
	s_cmp_lg_u32 0, -1
	v_or_b32_e32 v174, s10, v2
	s_cselect_b32 s10, 0, 0
	s_mov_b32 s36, 0
	s_mov_b32 s23, 0x20000
	s_mov_b32 s22, 0x40000
	s_add_i32 s33, s35, s10
	s_mov_b32 m0, s33
	s_nop 0
	buffer_load_dwordx4 v174, s[20:23], s36 offen lds
	s_mov_b32 s26, s22
	s_mov_b32 s27, s23
	s_add_i32 s34, s33, 0xc000
	s_mov_b32 m0, s34
	s_nop 0
	buffer_load_dwordx4 v174, s[24:27], s36 offen lds
	s_add_i32 s10, s33, 0x4000
	s_movk_i32 s37, 0x1000
	s_mov_b32 m0, s10
	s_nop 0
	buffer_load_dwordx4 v174, s[20:23], s37 offen lds
	s_add_i32 s10, s33, 0x8000
	s_movk_i32 s11, 0x2000
	s_mov_b32 m0, s10
	s_nop 0
	buffer_load_dwordx4 v174, s[20:23], s11 offen lds
	s_lshl_b32 s10, s2, 7
	s_and_b32 s10, s10, 0x380
	s_lshl_b32 s11, s31, 2
	s_add_i32 s10, s10, s11
	s_or_b32 s10, s30, s10
	v_and_b32_e32 v172, 31, v0
	v_lshl_or_b32 v140, s10, 7, v1
	v_mov_b32_e32 v141, 0
	v_lshl_add_u64 v[6:7], v[140:141], 4, s[14:15]
	v_ashrrev_i32_e32 v9, 31, v140
	v_mov_b32_e32 v8, v140
	v_lshl_or_b32 v140, s10, 5, v172
	v_lshlrev_b64 v[4:5], 2, v[140:141]
	v_lshl_add_u64 v[2:3], s[16:17], 0, v[4:5]
	global_load_dword v2, v[2:3], off
	v_lshl_add_u64 v[8:9], v[8:9], 4, s[14:15]
	global_load_dwordx4 v[116:119], v[6:7], off
	global_load_dwordx4 v[120:123], v[8:9], off offset:1024
	s_load_dwordx4 s[12:15], s[0:1], 0x40
	s_load_dwordx2 s[10:11], s[0:1], 0x50
	v_lshlrev_b32_e32 v173, 2, v1
	v_lshl_or_b32 v3, s28, 11, v173
	s_waitcnt lgkmcnt(0)
	global_load_dword v44, v3, s[14:15] offset:256
	global_load_dword v45, v3, s[14:15]
	v_bfe_u32 v175, v0, 5, 1
	v_lshlrev_b32_e32 v0, 11, v175
	v_lshlrev_b32_e32 v3, 4, v172
	s_add_i32 s0, s38, 0
	v_lshl_add_u64 v[4:5], s[12:13], 0, v[4:5]
	v_add3_u32 v176, s0, v0, v3
	global_load_dword v0, v[4:5], off
	v_lshrrev_b32_e32 v124, 2, v1
	v_lshrrev_b32_e32 v125, 4, v1
	v_xor_b32_e32 v124, v124, v125
	v_and_b32_e32 v124, 1, v124
	v_add_u32_e32 v124, -1, v124
	v_and_b32_e32 v124, 0x38383838, v124
	v_mov_b32_e32 v200, 0
	v_mov_b32_e32 v201, 0
	v_mov_b32_e32 v202, 0
	v_mov_b32_e32 v203, 0
	v_mov_b32_e32 v204, 0
	v_mov_b32_e32 v125, v124
	v_mov_b32_e32 v126, v124
	v_mov_b32_e32 v127, v124
	v_mov_b32_e32 v128, v124
	v_mov_b32_e32 v129, v124
	v_mov_b32_e32 v130, v124
	v_mov_b32_e32 v131, v124
	v_mov_b32_e32 v140, 0x7f7f7f7f
	s_mov_b32 s0, 0xf800000
	s_movk_i32 s15, 0x3000
	s_mov_b32 s12, -1
	s_movk_i32 s14, 0x4000
	s_mov_b32 s13, 0x8000
	v_mov_b32_e32 v132, v141
	v_mov_b32_e32 v133, v141
	v_mov_b32_e32 v134, v141
	v_mov_b32_e32 v135, v141
	v_mov_b32_e32 v136, v141
	v_mov_b32_e32 v137, v141
	v_mov_b32_e32 v138, v141
	v_mov_b32_e32 v139, v141
	v_mov_b32_e32 v52, v141
	v_mov_b32_e32 v53, v141
	v_mov_b32_e32 v54, v141
	v_mov_b32_e32 v55, v141
	v_mov_b32_e32 v56, v141
	v_mov_b32_e32 v57, v141
	v_mov_b32_e32 v58, v141
	v_mov_b32_e32 v59, v141
	v_mov_b32_e32 v60, v141
	v_mov_b32_e32 v61, v141
	v_mov_b32_e32 v62, v141
	v_mov_b32_e32 v63, v141
	v_mov_b32_e32 v64, v141
	v_mov_b32_e32 v65, v141
	v_mov_b32_e32 v66, v141
	v_mov_b32_e32 v67, v141
	s_waitcnt vmcnt(5)
	v_mov_b32_e32 v4, v2
	v_mov_b32_e32 v5, v2
	v_mov_b32_e32 v6, v2
	v_mov_b32_e32 v7, v2
	v_mov_b32_e32 v8, v2
	v_mov_b32_e32 v9, v2
	v_mov_b32_e32 v10, v2
	v_mov_b32_e32 v11, v2
	v_mov_b32_e32 v12, v2
	v_mov_b32_e32 v13, v2
	v_mov_b32_e32 v14, v2
	v_mov_b32_e32 v15, v2
	v_mov_b32_e32 v16, v2
	v_mov_b32_e32 v17, v2
	v_mov_b32_e32 v3, v2
	v_mov_b64_e32 v[18:19], v[16:17]
	v_mov_b64_e32 v[16:17], v[14:15]
	v_mov_b64_e32 v[14:15], v[12:13]
	v_mov_b64_e32 v[12:13], v[10:11]
	v_mov_b64_e32 v[10:11], v[8:9]
	v_mov_b64_e32 v[8:9], v[6:7]
	v_mov_b64_e32 v[6:7], v[4:5]
	v_mov_b64_e32 v[4:5], v[2:3]
	s_waitcnt vmcnt(0) lgkmcnt(0)
	s_barrier
	ds_read_b128 v[24:27], v176 offset:1024
	ds_read_b128 v[20:23], v176
	ds_read_b128 v[36:39], v176 offset:512
	ds_read_b128 v[40:43], v176 offset:1536
	s_waitcnt vmcnt(3) lgkmcnt(2)
	v_mfma_f32_32x32x64_f8f6f4 v[20:35], v[20:27], v[116:123], v[4:19]
	v_mbcnt_lo_u32_b32 v3, -1, 0
	v_mbcnt_hi_u32_b32 v46, -1, v3
	v_and_b32_e32 v3, 64, v46
	v_xor_b32_e32 v47, 32, v46
	v_add_u32_e32 v48, 64, v3
	s_waitcnt vmcnt(2)
	v_max_f32_e32 v3, v44, v44
	s_waitcnt vmcnt(1)
	v_max_f32_e32 v44, v45, v45
	v_max_f32_e32 v44, v44, v3
	v_cmp_lt_i32_e32 vcc, v47, v48
	s_waitcnt vmcnt(0) lgkmcnt(0)
	s_barrier
	s_mov_b32 m0, s33
	s_nop 0
	buffer_load_dwordx4 v174, s[20:23], s15 offen lds
	s_add_i32 s15, s34, 0x4000
	s_mov_b32 m0, s15
	s_nop 0
	buffer_load_dwordx4 v174, s[24:27], s37 offen lds
	ds_read_b128 v[84:87], v176 offset:16384
	ds_read_b128 v[92:95], v176 offset:16896
	ds_read_b128 v[88:91], v176 offset:17408
	ds_read_b128 v[96:99], v176 offset:17920
	s_waitcnt vmcnt(2) lgkmcnt(0)
	s_barrier
	s_waitcnt lgkmcnt(4)
	v_mfma_f32_32x32x64_f8f6f4 v[4:19], v[36:43], v[116:123], v[4:19]
	s_nop 1
	v_max_f32_e32 v3, v21, v21
	v_max_f32_e32 v36, v20, v20
	v_max_f32_e32 v3, v36, v3
	v_xor_b32_e32 v38, 16, v46
	s_nop 13
	v_max3_f32 v37, v22, v23, v5
	v_max3_f32 v36, v37, v26, v27
	v_cndmask_b32_e32 v37, v46, v47, vcc
	v_lshlrev_b32_e32 v37, 2, v37
	ds_bpermute_b32 v37, v37, v44
	v_cmp_lt_i32_e32 vcc, v38, v48
	v_max3_f32 v3, v3, v4, v6
	v_max3_f32 v3, v3, v7, v24
	v_cndmask_b32_e32 v38, v46, v38, vcc
	s_waitcnt lgkmcnt(0)
	v_max_f32_e32 v37, v37, v37
	v_max_f32_e32 v37, v44, v37
	v_lshlrev_b32_e32 v38, 2, v38
	ds_bpermute_b32 v38, v38, v37
	v_max3_f32 v36, v36, v10, v11
	v_max3_f32 v3, v3, v25, v8
	v_max3_f32 v36, v36, v30, v31
	v_max3_f32 v3, v3, v9, v28
	s_waitcnt lgkmcnt(0)
	v_max_f32_e32 v38, v38, v38
	v_max_f32_e32 v37, v37, v38
	v_xor_b32_e32 v38, 8, v46
	v_cmp_lt_i32_e32 vcc, v38, v48
	v_max3_f32 v36, v36, v14, v15
	v_max3_f32 v3, v3, v29, v12
	v_cndmask_b32_e32 v38, v46, v38, vcc
	v_lshlrev_b32_e32 v38, 2, v38
	ds_bpermute_b32 v38, v38, v37
	v_max3_f32 v36, v36, v34, v35
	v_max3_f32 v3, v3, v13, v32
	v_max3_f32 v36, v36, v18, v19
	v_max3_f32 v3, v3, v33, v16
	s_waitcnt lgkmcnt(0)
	v_max_f32_e32 v38, v38, v38
	v_max_f32_e32 v37, v37, v38
	v_xor_b32_e32 v38, 4, v46
	v_cmp_lt_i32_e32 vcc, v38, v48
	v_max3_f32 v3, v3, v17, v36
	v_mov_b32_e32 v36, v3
	v_cndmask_b32_e32 v38, v46, v38, vcc
	v_lshlrev_b32_e32 v38, 2, v38
	ds_bpermute_b32 v38, v38, v37
	v_permlane32_swap_b32_e32 v3, v36
	v_max_f32_e32 v36, v36, v36
	v_max_f32_e32 v3, v3, v3
	s_waitcnt lgkmcnt(0)
	v_max_f32_e32 v38, v38, v38
	v_max_f32_e32 v37, v37, v38
	v_xor_b32_e32 v38, 2, v46
	v_cmp_lt_i32_e32 vcc, v38, v48
	v_max_f32_e32 v3, v3, v36
	v_sub_f32_e32 v36, 0xc0400000, v3
	v_cndmask_b32_e32 v38, v46, v38, vcc
	v_lshlrev_b32_e32 v38, 2, v38
	ds_bpermute_b32 v38, v38, v37
	v_add_f32_e32 v20, v36, v20
	v_add_f32_e32 v21, v36, v21
	v_add_f32_e32 v22, v36, v22
	v_add_f32_e32 v23, v36, v23
	s_waitcnt lgkmcnt(0)
	v_max_f32_e32 v38, v38, v38
	v_max_f32_e32 v37, v37, v38
	v_xor_b32_e32 v38, 1, v46
	v_cmp_lt_i32_e32 vcc, v38, v48
	v_add_f32_e32 v24, v36, v24
	v_add_f32_e32 v25, v36, v25
	v_cndmask_b32_e32 v38, v46, v38, vcc
	v_lshlrev_b32_e32 v38, 2, v38
	ds_bpermute_b32 v38, v38, v37
	v_add_f32_e32 v26, v36, v26
	v_add_f32_e32 v27, v36, v27
	v_add_f32_e32 v28, v36, v28
	v_add_f32_e32 v29, v36, v29
	s_waitcnt lgkmcnt(0)
	v_max_f32_e32 v38, v38, v38
	v_max_f32_e32 v37, v37, v38
	v_mul_f32_e32 v38, 0x4f800000, v37
	v_cmp_gt_f32_e32 vcc, s0, v37
	v_add_f32_e32 v30, v36, v30
	v_add_f32_e32 v31, v36, v31
	v_cndmask_b32_e32 v37, v37, v38, vcc
	v_sqrt_f32_e32 v38, v37
	v_add_f32_e32 v32, v36, v32
	v_add_f32_e32 v33, v36, v33
	v_add_f32_e32 v34, v36, v34
	v_add_f32_e32 v35, v36, v35
	v_add_f32_e32 v4, v36, v4
	v_add_f32_e32 v5, v36, v5
	v_add_f32_e32 v6, v36, v6
	v_add_f32_e32 v7, v36, v7
	v_add_f32_e32 v8, v36, v8
	v_add_f32_e32 v9, v36, v9
	v_add_f32_e32 v10, v36, v10
	v_add_f32_e32 v11, v36, v11
	v_add_f32_e32 v12, v36, v12
	v_add_f32_e32 v13, v36, v13
	v_add_f32_e32 v14, v36, v14
	v_add_f32_e32 v15, v36, v15
	v_add_f32_e32 v16, v36, v16
	v_add_f32_e32 v17, v36, v17
	v_add_f32_e32 v18, v36, v18
	v_add_f32_e32 v19, v36, v19
	v_add_u32_e32 v36, -1, v38
	v_fma_f32 v39, -v36, v38, v37
	v_cmp_ge_f32_e64 s[0:1], 0, v39
	v_add_u32_e32 v39, 1, v38
	v_exp_f32_e32 v161, v20
	v_cndmask_b32_e64 v36, v38, v36, s[0:1]
	v_fma_f32 v38, -v39, v38, v37
	v_cmp_lt_f32_e64 s[0:1], 0, v38
	v_exp_f32_e32 v100, v4
	v_exp_f32_e32 v163, v21
	v_cndmask_b32_e64 v36, v36, v39, s[0:1]
	v_mul_f32_e32 v38, 0x37800000, v36
	v_cndmask_b32_e32 v36, v36, v38, vcc
	v_mov_b32_e32 v38, 0x260
	v_cmp_class_f32_e32 vcc, v37, v38
	s_mov_b32 s0, 0x42700000
	v_exp_f32_e32 v148, v5
	v_cndmask_b32_e32 v36, v36, v37, vcc
	s_waitcnt vmcnt(0)
	v_mul_f32_e32 v0, v36, v0
	v_mul_f32_e32 v0, 0x3f91eb85, v0
	v_exp_f32_e32 v162, v22
	v_exp_f32_e32 v101, v6
	v_exp_f32_e32 v164, v23
	v_exp_f32_e32 v102, v7
	v_exp_f32_e32 v150, v24
	v_exp_f32_e32 v143, v8
	v_exp_f32_e32 v154, v25
	v_exp_f32_e32 v146, v9
	v_exp_f32_e32 v152, v26
	v_exp_f32_e32 v145, v10
	v_exp_f32_e32 v157, v27
	v_exp_f32_e32 v147, v11
	v_exp_f32_e32 v149, v28
	v_exp_f32_e32 v69, v12
	v_exp_f32_e32 v153, v29
	v_exp_f32_e32 v109, v13
	v_exp_f32_e32 v151, v30
	v_exp_f32_e32 v108, v14
	v_exp_f32_e32 v156, v31
	v_exp_f32_e32 v142, v15
	v_exp_f32_e32 v155, v32
	v_exp_f32_e32 v110, v16
	v_exp_f32_e32 v159, v33
	v_exp_f32_e32 v144, v17
	v_exp_f32_e32 v158, v34
	v_exp_f32_e32 v111, v18
	v_exp_f32_e32 v160, v35
	v_exp_f32_e32 v114, v19
	v_cmp_nge_f32_e64 s[0:1], s0, v0
	v_sub_f32_e32 v0, v2, v3
	v_add_f32_e32 v36, 0xc0400000, v0
	v_mov_b32_e32 v37, v36
	v_mov_b32_e32 v38, v36
	v_mov_b32_e32 v39, v36
	v_mov_b32_e32 v40, v36
	v_mov_b32_e32 v41, v36
	v_mov_b32_e32 v42, v36
	v_mov_b32_e32 v43, v36
	v_mov_b32_e32 v44, v36
	v_mov_b32_e32 v45, v36
	v_mov_b32_e32 v46, v36
	v_mov_b32_e32 v47, v36
	v_mov_b32_e32 v48, v36
	v_mov_b32_e32 v49, v36
	v_mov_b32_e32 v50, v36
	v_mov_b32_e32 v51, v36
	v_mov_b32_e32 v4, v141
	v_mov_b32_e32 v5, v141
	v_mov_b32_e32 v6, v141
	v_mov_b32_e32 v7, v141
	v_mov_b32_e32 v8, v141
	v_mov_b32_e32 v9, v141
	v_mov_b32_e32 v10, v141
	v_mov_b32_e32 v11, v141
	v_mov_b32_e32 v12, v141
	v_mov_b32_e32 v13, v141
	v_mov_b32_e32 v14, v141
	v_mov_b32_e32 v15, v141
	v_mov_b32_e32 v16, v141
	v_mov_b32_e32 v17, v141
	v_mov_b32_e32 v18, v141
	v_mov_b32_e32 v19, v141
	v_mov_b32_e32 v20, v141
	v_mov_b32_e32 v21, v141
	v_mov_b32_e32 v22, v141
	v_mov_b32_e32 v23, v141
	v_mov_b32_e32 v24, v141
	v_mov_b32_e32 v25, v141
	v_mov_b32_e32 v26, v141
	v_mov_b32_e32 v27, v141
	v_mov_b32_e32 v28, v141
	v_mov_b32_e32 v29, v141
	v_mov_b32_e32 v30, v141
	v_mov_b32_e32 v31, v141
	v_mov_b32_e32 v32, v141
	v_mov_b32_e32 v33, v141
	v_mov_b32_e32 v34, v141
	v_mov_b32_e32 v35, v141
	v_mov_b32_e32 v0, v141
.LBB1_1:
	s_add_i32 s12, s12, 2
	s_waitcnt lgkmcnt(2)
	v_mfma_f32_32x32x64_f8f6f4 v[76:91], v[84:91], v[116:123], v[36:51]
	v_cvt_pk_fp8_f32 v132, v161, v163
	v_add_u32_e32 v68, s36, v176
	v_cvt_pk_fp8_f32 v132, v162, v164 op_sel:[0,0,1]
	ds_read_b128 v[162:165], v68 offset:49152
	ds_read_b128 v[166:169], v68 offset:50176
	v_cvt_pk_fp8_f32 v133, v150, v154
	v_cvt_pk_fp8_f32 v133, v152, v157 op_sel:[0,0,1]
	s_lshl_b32 s16, s12, 12
	s_add_i32 s15, s16, 0x3000
	s_add_i32 s17, s14, s33
	s_mov_b32 m0, s17
	s_nop 0
	buffer_load_dwordx4 v174, s[20:23], s15 offen lds
	v_cvt_pk_fp8_f32 v134, v149, v153
	v_cvt_pk_fp8_f32 v134, v151, v156 op_sel:[0,0,1]
	v_cvt_pk_fp8_f32 v135, v155, v159
	v_cvt_pk_fp8_f32 v135, v158, v160 op_sel:[0,0,1]
	v_cvt_pk_fp8_f32 v136, v100, v148
	v_cvt_pk_fp8_f32 v136, v101, v102 op_sel:[0,0,1]
	s_waitcnt lgkmcnt(2)
	v_mfma_f32_32x32x64_f8f6f4 v[92:107], v[92:99], v[116:123], v[36:51]
	ds_read_b128 v[148:151], v68 offset:49664
	ds_read_b128 v[152:155], v68 offset:50688
	v_cvt_pk_fp8_f32 v137, v143, v146
	v_cvt_pk_fp8_f32 v137, v145, v147 op_sel:[0,0,1]
	s_add_i32 s15, s16, 0x1000
	s_add_i32 s17, s13, s34
	s_mov_b32 m0, s17
	s_nop 0
	buffer_load_dwordx4 v174, s[24:27], s15 offen lds
	v_cvt_pk_fp8_f32 v138, v69, v109
	v_cvt_pk_fp8_f32 v138, v108, v142 op_sel:[0,0,1]
	v_cvt_pk_fp8_f32 v139, v110, v144
	v_cvt_pk_fp8_f32 v139, v111, v114 op_sel:[0,0,1]
	s_waitcnt lgkmcnt(2)
	s_nop 0
	v_mfma_f32_32x32x64_f8f6f4 v[4:19], v[162:169], v[132:139], v[4:19]
	v_exp_f32_e32 v142, v76
	v_exp_f32_e32 v143, v77
	v_exp_f32_e32 v144, v78
	v_exp_f32_e32 v145, v79
	v_exp_f32_e32 v146, v80
	v_exp_f32_e32 v147, v81
	v_exp_f32_e32 v156, v82
	v_exp_f32_e32 v157, v83
	v_add_u32_e32 v158, s13, v176
	ds_read_b128 v[108:111], v158
	ds_read_b128 v[112:115], v158 offset:1024
	ds_read_b128 v[52:55], v158 offset:512
	ds_read_b128 v[56:59], v158 offset:1536
	v_exp_f32_e32 v159, v84
	v_exp_f32_e32 v160, v85
	v_mfma_f32_16x16x128_f8f6f4 v[200:203], v[124:131], v[132:139], v[200:203]
	v_exp_f32_e32 v161, v86
	v_exp_f32_e32 v162, v87
	v_exp_f32_e32 v163, v88
	v_exp_f32_e32 v164, v89
	v_exp_f32_e32 v165, v90
	v_exp_f32_e32 v166, v91
	s_waitcnt lgkmcnt(4)
	v_mfma_f32_32x32x64_f8f6f4 v[20:35], v[148:155], v[132:139], v[20:35]
	v_exp_f32_e32 v167, v92
	v_exp_f32_e32 v168, v93
	v_exp_f32_e32 v169, v94
	v_exp_f32_e32 v170, v95
	v_exp_f32_e32 v148, v96
	v_exp_f32_e32 v149, v97
	v_exp_f32_e32 v150, v98
	v_exp_f32_e32 v151, v99
	v_exp_f32_e32 v152, v100
	v_exp_f32_e32 v153, v101
	v_exp_f32_e32 v154, v102
	v_exp_f32_e32 v155, v103
	v_exp_f32_e32 v158, v104
	v_exp_f32_e32 v171, v105
	v_exp_f32_e32 v177, v106
	v_exp_f32_e32 v186, v107
	s_waitcnt vmcnt(2) lgkmcnt(0)
	s_barrier
	s_add_i32 s15, s13, 0x4000
	s_cmpk_lg_u32 s13, 0x8000
	s_cselect_b32 s15, s15, 0
	s_waitcnt lgkmcnt(2)
	v_mfma_f32_32x32x64_f8f6f4 v[84:99], v[108:115], v[116:123], v[36:51]
	v_cvt_pk_fp8_f32 v132, v142, v143
	v_add_u32_e32 v142, s14, v176
	v_cvt_pk_fp8_f32 v132, v144, v145 op_sel:[0,0,1]
	ds_read_b128 v[60:63], v142 offset:49152
	ds_read_b128 v[64:67], v142 offset:50176
	v_cvt_pk_fp8_f32 v133, v146, v147
	v_cvt_pk_fp8_f32 v133, v156, v157 op_sel:[0,0,1]
	s_add_i32 s14, s16, 0x4000
	s_add_i32 s17, s13, s33
	s_mov_b32 m0, s17
	s_nop 0
	buffer_load_dwordx4 v174, s[20:23], s14 offen lds
	v_cvt_pk_fp8_f32 v134, v159, v160
	v_cvt_pk_fp8_f32 v134, v161, v162 op_sel:[0,0,1]
	v_cvt_pk_fp8_f32 v135, v163, v164
	v_cvt_pk_fp8_f32 v135, v165, v166 op_sel:[0,0,1]
	s_waitcnt lgkmcnt(2)
	v_mfma_f32_32x32x64_f8f6f4 v[100:115], v[52:59], v[116:123], v[36:51]
	v_cvt_pk_fp8_f32 v136, v167, v168
	v_cvt_pk_fp8_f32 v136, v169, v170 op_sel:[0,0,1]
	ds_read_b128 v[178:181], v142 offset:49664
	ds_read_b128 v[182:185], v142 offset:50688
	v_cvt_pk_fp8_f32 v137, v148, v149
	v_cvt_pk_fp8_f32 v137, v150, v151 op_sel:[0,0,1]
	s_addk_i32 s16, 0x2000
	s_add_i32 s14, s15, s34
	s_mov_b32 m0, s14
	s_nop 0
	buffer_load_dwordx4 v174, s[24:27], s16 offen lds
	v_cvt_pk_fp8_f32 v138, v152, v153
	v_cvt_pk_fp8_f32 v138, v154, v155 op_sel:[0,0,1]
	v_cvt_pk_fp8_f32 v139, v158, v171
	v_cvt_pk_fp8_f32 v139, v177, v186 op_sel:[0,0,1]
	v_sub_f32_e32 v52, v200, v204
	v_mov_b32_e32 v204, v200
	v_max_f32_e32 v0, v0, v0
	v_max_f32_e32 v0, v0, v52
	s_waitcnt lgkmcnt(2)
	v_mfma_f32_32x32x64_f8f6f4 v[4:19], v[60:67], v[132:139], v[4:19]
	v_exp_f32_e32 v161, v84
	v_exp_f32_e32 v163, v85
	v_exp_f32_e32 v162, v86
	v_exp_f32_e32 v164, v87
	v_exp_f32_e32 v150, v88
	v_exp_f32_e32 v154, v89
	v_exp_f32_e32 v152, v90
	v_exp_f32_e32 v157, v91
	v_add_u32_e32 v141, s15, v176
	ds_read_b128 v[84:87], v141
	ds_read_b128 v[88:91], v141 offset:1024
	v_mfma_f32_16x16x128_f8f6f4 v[200:203], v[124:131], v[132:139], v[200:203]
	v_exp_f32_e32 v149, v92
	v_exp_f32_e32 v153, v93
	v_exp_f32_e32 v151, v94
	v_exp_f32_e32 v156, v95
	v_exp_f32_e32 v155, v96
	v_exp_f32_e32 v159, v97
	v_exp_f32_e32 v158, v98
	v_exp_f32_e32 v160, v99
	ds_read_b128 v[92:95], v141 offset:512
	ds_read_b128 v[96:99], v141 offset:1536
	s_waitcnt lgkmcnt(4)
	v_mfma_f32_32x32x64_f8f6f4 v[20:35], v[178:185], v[132:139], v[20:35]
	v_exp_f32_e32 v100, v100
	v_exp_f32_e32 v148, v101
	v_exp_f32_e32 v101, v102
	v_exp_f32_e32 v102, v103
	v_exp_f32_e32 v143, v104
	v_exp_f32_e32 v146, v105
	v_exp_f32_e32 v145, v106
	v_exp_f32_e32 v147, v107
	v_exp_f32_e32 v69, v108
	v_exp_f32_e32 v109, v109
	v_exp_f32_e32 v108, v110
	v_exp_f32_e32 v142, v111
	v_exp_f32_e32 v110, v112
	v_exp_f32_e32 v144, v113
	v_exp_f32_e32 v111, v114
	v_exp_f32_e32 v114, v115
	s_waitcnt vmcnt(2) lgkmcnt(0)
	s_barrier
	s_add_i32 s16, s15, 0x4000
	s_cmpk_lg_u32 s15, 0x8000
	s_mov_b32 s36, s13
	s_mov_b32 s14, s15
	s_cselect_b32 s13, s16, 0
	s_cmp_gt_u32 s12, 24
	s_cbranch_scc0 .LBB1_1
	v_add_u32_e32 v113, 0xc000, v176
	v_mov_b32_e32 v112, 0x7f7f7f7f
	v_cvt_pk_fp8_f32 v132, v161, v163
	v_cvt_pk_fp8_f32 v132, v162, v164 op_sel:[0,0,1]
	s_waitcnt lgkmcnt(2)
	v_mfma_f32_32x32x64_f8f6f4 v[70:85], v[84:91], v[116:123], v[36:51]
	ds_read_b128 v[162:165], v113 offset:32768
	ds_read_b128 v[166:169], v113 offset:33792
	v_cvt_pk_fp8_f32 v133, v150, v154
	v_cvt_pk_fp8_f32 v133, v152, v157 op_sel:[0,0,1]
	s_mov_b32 s13, 0x1e000
	s_mov_b32 m0, s33
	s_nop 0
	buffer_load_dwordx4 v174, s[20:23], s13 offen lds
	v_cvt_pk_fp8_f32 v134, v149, v153
	v_cvt_pk_fp8_f32 v134, v151, v156 op_sel:[0,0,1]
	v_cvt_pk_fp8_f32 v135, v155, v159
	v_cvt_pk_fp8_f32 v135, v158, v160 op_sel:[0,0,1]
	v_cvt_pk_fp8_f32 v136, v100, v148
	v_cvt_pk_fp8_f32 v136, v101, v102 op_sel:[0,0,1]
	s_waitcnt lgkmcnt(2)
	v_mfma_f32_32x32x64_f8f6f4 v[86:101], v[92:99], v[116:123], v[36:51]
	ds_read_b128 v[148:151], v113 offset:33280
	ds_read_b128 v[152:155], v113 offset:34304
	v_cvt_pk_fp8_f32 v137, v143, v146
	v_cvt_pk_fp8_f32 v137, v145, v147 op_sel:[0,0,1]
	s_cmp_lg_u32 0, -1
	s_cselect_b32 s12, 0, 0
	s_add_i32 s15, s12, s35
	s_add_i32 s12, s15, 0x10000
	s_mov_b32 s26, s22
	s_mov_b32 s27, s23
	s_mov_b32 s14, 0x1c000
	s_mov_b32 m0, s12
	s_nop 0
	buffer_load_dwordx4 v174, s[24:27], s14 offen lds
	v_cvt_pk_fp8_f32 v138, v69, v109
	v_cvt_pk_fp8_f32 v138, v108, v142 op_sel:[0,0,1]
	v_cvt_pk_fp8_f32 v139, v110, v144
	v_cvt_pk_fp8_f32 v139, v111, v114 op_sel:[0,0,1]
	s_waitcnt lgkmcnt(2)
	s_nop 0
	v_mfma_f32_32x32x64_f8f6f4 v[4:19], v[162:169], v[132:139], v[4:19]
	v_exp_f32_e32 v104, v73
	v_exp_f32_e32 v69, v70
	v_exp_f32_e32 v102, v71
	v_exp_f32_e32 v103, v72
	v_exp_f32_e32 v110, v74
	v_exp_f32_e32 v111, v75
	v_exp_f32_e32 v114, v76
	v_exp_f32_e32 v115, v77
	ds_read_b128 v[70:73], v176 offset:16384
	ds_read_b128 v[74:77], v176 offset:17408
	v_mfma_f32_16x16x128_f8f6f4 v[200:203], v[124:131], v[132:139], v[200:203]
	v_exp_f32_e32 v140, v78
	v_exp_f32_e32 v141, v79
	v_exp_f32_e32 v142, v80
	v_exp_f32_e32 v143, v81
	v_exp_f32_e32 v144, v82
	v_exp_f32_e32 v145, v83
	v_exp_f32_e32 v146, v84
	v_exp_f32_e32 v147, v85
	s_waitcnt lgkmcnt(2)
	v_mfma_f32_32x32x64_f8f6f4 v[20:35], v[148:155], v[132:139], v[20:35]
	v_exp_f32_e32 v156, v86
	v_exp_f32_e32 v157, v87
	v_exp_f32_e32 v158, v88
	v_exp_f32_e32 v159, v89
	v_exp_f32_e32 v148, v90
	v_exp_f32_e32 v149, v91
	v_exp_f32_e32 v150, v92
	v_exp_f32_e32 v151, v93
	ds_read_b128 v[86:89], v176 offset:16896
	ds_read_b128 v[90:93], v176 offset:17920
	v_exp_f32_e32 v152, v94
	v_exp_f32_e32 v153, v95
	v_exp_f32_e32 v154, v96
	v_exp_f32_e32 v155, v97
	v_exp_f32_e32 v160, v98
	v_exp_f32_e32 v161, v99
	v_exp_f32_e32 v162, v100
	v_exp_f32_e32 v163, v101
	s_waitcnt vmcnt(2) lgkmcnt(0)
	s_barrier
	s_waitcnt lgkmcnt(2)
	v_mfma_f32_32x32x64_f8f6f4 v[70:85], v[70:77], v[116:123], v[36:51]
	v_cvt_pk_fp8_f32 v132, v69, v102
	v_cvt_pk_fp8_f32 v132, v103, v104 op_sel:[0,0,1]
	ds_read_b128 v[102:105], v176 offset:49152
	ds_read_b128 v[106:109], v176 offset:50176
	v_cvt_pk_fp8_f32 v133, v110, v111
	v_cvt_pk_fp8_f32 v133, v114, v115 op_sel:[0,0,1]
	s_add_i32 s16, s15, 0x4000
	s_mov_b32 s14, 0x1f000
	s_mov_b32 m0, s16
	s_nop 0
	buffer_load_dwordx4 v174, s[20:23], s14 offen lds
	v_cvt_pk_fp8_f32 v134, v140, v141
	v_cvt_pk_fp8_f32 v134, v142, v143 op_sel:[0,0,1]
	v_cvt_pk_fp8_f32 v135, v144, v145
	v_cvt_pk_fp8_f32 v135, v146, v147 op_sel:[0,0,1]
	s_waitcnt lgkmcnt(2)
	v_mfma_f32_32x32x64_f8f6f4 v[86:101], v[86:93], v[116:123], v[36:51]
	v_cvt_pk_fp8_f32 v136, v156, v157
	v_cvt_pk_fp8_f32 v136, v158, v159 op_sel:[0,0,1]
	ds_read_b128 v[140:143], v176 offset:49664
	ds_read_b128 v[144:147], v176 offset:50688
	v_cvt_pk_fp8_f32 v137, v148, v149
	v_cvt_pk_fp8_f32 v137, v150, v151 op_sel:[0,0,1]
	s_add_i32 s15, s15, 0x14000
	s_mov_b32 s16, 0x1d000
	s_mov_b32 m0, s15
	s_nop 0
	buffer_load_dwordx4 v174, s[24:27], s16 offen lds
	v_cvt_pk_fp8_f32 v138, v152, v153
	v_cvt_pk_fp8_f32 v138, v154, v155 op_sel:[0,0,1]
	v_cvt_pk_fp8_f32 v139, v160, v161
	v_cvt_pk_fp8_f32 v139, v162, v163 op_sel:[0,0,1]
	v_sub_f32_e32 v114, v200, v204
	v_mov_b32_e32 v204, v200
	s_waitcnt lgkmcnt(2)
	v_mfma_f32_32x32x64_f8f6f4 v[4:19], v[102:109], v[132:139], v[4:19]
	v_exp_f32_e32 v110, v70
	v_exp_f32_e32 v111, v71
	v_exp_f32_e32 v148, v73
	v_exp_f32_e32 v115, v72
	v_exp_f32_e32 v149, v74
	v_exp_f32_e32 v150, v75
	v_exp_f32_e32 v151, v76
	v_exp_f32_e32 v152, v77
	ds_read_b128 v[70:73], v176 offset:32768
	ds_read_b128 v[74:77], v176 offset:33792
	v_mfma_f32_16x16x128_f8f6f4 v[200:203], v[124:131], v[132:139], v[200:203]
	v_exp_f32_e32 v153, v78
	v_exp_f32_e32 v154, v79
	v_exp_f32_e32 v155, v80
	v_exp_f32_e32 v156, v81
	v_exp_f32_e32 v157, v83
	v_exp_f32_e32 v158, v84
	v_exp_f32_e32 v159, v85
	s_nop 7
	v_exp_f32_e32 v53, v82
	s_waitcnt lgkmcnt(2)
	v_mfma_f32_32x32x64_f8f6f4 v[20:35], v[140:147], v[132:139], v[20:35]
	v_exp_f32_e32 v160, v86
	v_exp_f32_e32 v161, v87
	v_exp_f32_e32 v162, v88
	v_exp_f32_e32 v163, v89
	v_exp_f32_e32 v164, v90
	v_exp_f32_e32 v165, v91
	v_exp_f32_e32 v166, v92
	v_exp_f32_e32 v167, v93
	ds_read_b128 v[78:81], v176 offset:33280
	ds_read_b128 v[82:85], v176 offset:34304
	v_exp_f32_e32 v168, v94
	v_exp_f32_e32 v169, v95
	v_exp_f32_e32 v170, v96
	v_exp_f32_e32 v171, v97
	v_exp_f32_e32 v177, v98
	v_exp_f32_e32 v178, v99
	v_exp_f32_e32 v179, v100
	v_exp_f32_e32 v180, v101
	s_waitcnt vmcnt(2) lgkmcnt(0)
	s_barrier
	s_waitcnt lgkmcnt(2)
	v_mfma_f32_32x32x64_f8f6f4 v[86:101], v[70:77], v[116:123], v[36:51]
	v_cvt_pk_fp8_f32 v132, v110, v111
	v_cvt_pk_fp8_f32 v132, v115, v148 op_sel:[0,0,1]
	ds_read_b128 v[102:105], v113 offset:16384
	ds_read_b128 v[106:109], v113 offset:17408
	v_cvt_pk_fp8_f32 v133, v149, v150
	v_cvt_pk_fp8_f32 v133, v151, v152 op_sel:[0,0,1]
	v_cvt_pk_fp8_f32 v134, v153, v154
	v_cvt_pk_fp8_f32 v134, v155, v156 op_sel:[0,0,1]
	v_cvt_pk_fp8_f32 v135, v53, v157
	v_cvt_pk_fp8_f32 v135, v158, v159 op_sel:[0,0,1]
	s_waitcnt lgkmcnt(2)
	v_mfma_f32_32x32x64_f8f6f4 v[70:85], v[78:85], v[116:123], v[36:51]
	v_cvt_pk_fp8_f32 v136, v160, v161
	v_cvt_pk_fp8_f32 v136, v162, v163 op_sel:[0,0,1]
	ds_read_b128 v[140:143], v113 offset:16896
	ds_read_b128 v[144:147], v113 offset:17920
	v_cvt_pk_fp8_f32 v137, v164, v165
	v_cvt_pk_fp8_f32 v137, v166, v167 op_sel:[0,0,1]
	s_mov_b32 m0, s34
	s_nop 0
	buffer_load_dwordx4 v174, s[24:27], s13 offen lds
	v_cvt_pk_fp8_f32 v138, v168, v169
	v_cvt_pk_fp8_f32 v138, v170, v171 op_sel:[0,0,1]
	v_cvt_pk_fp8_f32 v139, v177, v178
	v_cvt_pk_fp8_f32 v139, v179, v180 op_sel:[0,0,1]
	s_waitcnt lgkmcnt(2)
	s_nop 0
	v_mfma_f32_32x32x64_f8f6f4 v[4:19], v[102:109], v[132:139], v[4:19]
	v_exp_f32_e32 v148, v88
	v_exp_f32_e32 v149, v89
	v_exp_f32_e32 v53, v86
	v_exp_f32_e32 v115, v87
	v_exp_f32_e32 v150, v92
	v_exp_f32_e32 v151, v93
	v_exp_f32_e32 v102, v90
	v_exp_f32_e32 v103, v91
	ds_read_b128 v[86:89], v176
	ds_read_b128 v[90:93], v176 offset:1024
	v_mfma_f32_16x16x128_f8f6f4 v[200:203], v[124:131], v[132:139], v[200:203]
	v_exp_f32_e32 v152, v94
	v_exp_f32_e32 v153, v95
	v_exp_f32_e32 v154, v96
	v_exp_f32_e32 v155, v97
	v_exp_f32_e32 v156, v98
	v_exp_f32_e32 v157, v99
	v_exp_f32_e32 v158, v100
	v_exp_f32_e32 v159, v101
	s_waitcnt lgkmcnt(2)
	v_mfma_f32_32x32x64_f8f6f4 v[20:35], v[140:147], v[132:139], v[20:35]
	v_exp_f32_e32 v160, v70
	v_exp_f32_e32 v161, v71
	v_exp_f32_e32 v162, v72
	v_exp_f32_e32 v163, v73
	v_exp_f32_e32 v164, v74
	v_exp_f32_e32 v165, v75
	v_exp_f32_e32 v166, v76
	v_exp_f32_e32 v167, v77
	ds_read_b128 v[94:97], v176 offset:512
	ds_read_b128 v[98:101], v176 offset:1536
	v_exp_f32_e32 v168, v78
	v_exp_f32_e32 v169, v79
	v_exp_f32_e32 v170, v80
	v_exp_f32_e32 v171, v81
	v_exp_f32_e32 v177, v82
	v_exp_f32_e32 v178, v83
	v_exp_f32_e32 v179, v84
	v_exp_f32_e32 v180, v85
	s_waitcnt vmcnt(1) lgkmcnt(0)
	s_barrier
	s_waitcnt lgkmcnt(2)
	v_mfma_f32_32x32x64_f8f6f4 v[70:85], v[86:93], v[116:123], v[36:51]
	ds_read_b128 v[104:107], v113 offset:32768
	ds_read_b128 v[108:111], v113 offset:33792
	v_cvt_pk_fp8_f32 v132, v53, v115
	v_cvt_pk_fp8_f32 v133, v102, v103
	v_cvt_pk_fp8_f32 v134, v152, v153
	v_cvt_pk_fp8_f32 v132, v148, v149 op_sel:[0,0,1]
	v_cvt_pk_fp8_f32 v133, v150, v151 op_sel:[0,0,1]
	v_cvt_pk_fp8_f32 v134, v154, v155 op_sel:[0,0,1]
	v_cvt_pk_fp8_f32 v135, v156, v157
	v_cvt_pk_fp8_f32 v135, v158, v159 op_sel:[0,0,1]
	s_waitcnt lgkmcnt(2)
	v_mfma_f32_32x32x64_f8f6f4 v[86:101], v[94:101], v[116:123], v[36:51]
	v_cvt_pk_fp8_f32 v136, v160, v161
	v_cvt_pk_fp8_f32 v136, v162, v163 op_sel:[0,0,1]
	ds_read_b128 v[140:143], v113 offset:33280
	ds_read_b128 v[144:147], v113 offset:34304
	v_cvt_pk_fp8_f32 v137, v164, v165
	v_cvt_pk_fp8_f32 v137, v166, v167 op_sel:[0,0,1]
	s_mov_b32 m0, s12
	s_nop 0
	buffer_load_dwordx4 v174, s[24:27], s14 offen lds
	v_cvt_pk_fp8_f32 v138, v168, v169
	v_cvt_pk_fp8_f32 v138, v170, v171 op_sel:[0,0,1]
	v_cvt_pk_fp8_f32 v139, v177, v178
	v_cvt_pk_fp8_f32 v139, v179, v180 op_sel:[0,0,1]
	v_sub_f32_e32 v52, v200, v204
	v_mov_b32_e32 v204, v200
	v_max3_f32 v0, v0, v114, v52
	v_exp_f32_e32 v72, v72
	v_exp_f32_e32 v73, v73
	v_exp_f32_e32 v52, v70
	v_exp_f32_e32 v53, v71
	v_exp_f32_e32 v102, v74
	v_exp_f32_e32 v103, v75
	v_exp_f32_e32 v114, v76
	v_exp_f32_e32 v115, v77
	ds_read_b128 v[150:153], v176 offset:16384
	ds_read_b128 v[154:157], v176 offset:17408
	v_mfma_f32_16x16x128_f8f6f4 v[200:203], v[124:131], v[132:139], v[200:203]
	v_exp_f32_e32 v177, v78
	v_exp_f32_e32 v178, v79
	v_exp_f32_e32 v179, v80
	v_exp_f32_e32 v180, v81
	s_nop 10
	v_exp_f32_e32 v55, v82
	v_exp_f32_e32 v181, v83
	v_exp_f32_e32 v182, v84
	v_exp_f32_e32 v183, v85
	v_exp_f32_e32 v184, v86
	v_exp_f32_e32 v185, v87
	v_exp_f32_e32 v88, v88
	v_exp_f32_e32 v89, v89
	v_exp_f32_e32 v186, v90
	v_exp_f32_e32 v187, v91
	v_exp_f32_e32 v188, v92
	v_exp_f32_e32 v189, v93
	ds_read_b128 v[164:167], v176 offset:16896
	ds_read_b128 v[168:171], v176 offset:17920
	v_exp_f32_e32 v190, v94
	v_exp_f32_e32 v191, v95
	v_exp_f32_e32 v192, v96
	v_exp_f32_e32 v193, v97
	v_exp_f32_e32 v194, v98
	v_exp_f32_e32 v195, v99
	v_exp_f32_e32 v196, v100
	v_exp_f32_e32 v197, v101
	s_waitcnt vmcnt(0) lgkmcnt(0)
	s_barrier
	v_mov_b32_e32 v148, v132
	v_cvt_pk_fp8_f32 v148, v52, v53
	v_cvt_pk_fp8_f32 v148, v72, v73 op_sel:[0,0,1]
	s_waitcnt lgkmcnt(2)
	v_mfma_f32_32x32x64_f8f6f4 v[72:87], v[150:157], v[116:123], v[36:51]
	ds_read_b128 v[156:159], v176 offset:49152
	ds_read_b128 v[160:163], v176 offset:50176
	v_mov_b32_e32 v149, v133
	v_cvt_pk_fp8_f32 v149, v102, v103
	v_cvt_pk_fp8_f32 v149, v114, v115 op_sel:[0,0,1]
	v_mov_b32_e32 v150, v134
	v_cvt_pk_fp8_f32 v150, v177, v178
	v_cvt_pk_fp8_f32 v150, v179, v180 op_sel:[0,0,1]
	v_mov_b32_e32 v151, v135
	v_cvt_pk_fp8_f32 v151, v55, v181
	v_cvt_pk_fp8_f32 v151, v182, v183 op_sel:[0,0,1]
	v_mov_b32_e32 v152, v136
	v_cvt_pk_fp8_f32 v152, v184, v185
	v_cvt_pk_fp8_f32 v152, v88, v89 op_sel:[0,0,1]
	s_waitcnt lgkmcnt(2)
	v_mfma_f32_32x32x64_f8f6f4 v[88:103], v[164:171], v[116:123], v[36:51]
	ds_read_b128 v[164:167], v176 offset:49664
	ds_read_b128 v[168:171], v176 offset:50688
	v_mov_b32_e32 v153, v137
	v_cvt_pk_fp8_f32 v153, v186, v187
	v_cvt_pk_fp8_f32 v153, v188, v189 op_sel:[0,0,1]
	v_mov_b32_e32 v154, v138
	v_cvt_pk_fp8_f32 v154, v190, v191
	v_cvt_pk_fp8_f32 v154, v192, v193 op_sel:[0,0,1]
	v_mov_b32_e32 v155, v139
	v_cvt_pk_fp8_f32 v155, v194, v195
	v_cvt_pk_fp8_f32 v155, v196, v197 op_sel:[0,0,1]
	v_sub_f32_e32 v52, v200, v204
	v_mov_b32_e32 v204, v200
	s_nop 2
	v_exp_f32_e32 v36, v72
	v_exp_f32_e32 v37, v73
	v_exp_f32_e32 v38, v74
	v_exp_f32_e32 v39, v75
	v_exp_f32_e32 v40, v76
	v_exp_f32_e32 v41, v77
	v_exp_f32_e32 v42, v78
	v_exp_f32_e32 v43, v79
	v_exp_f32_e32 v53, v80
	v_exp_f32_e32 v80, v83
	v_exp_f32_e32 v54, v81
	v_exp_f32_e32 v55, v82
	v_exp_f32_e32 v81, v84
	v_exp_f32_e32 v82, v85
	v_exp_f32_e32 v83, v86
	v_exp_f32_e32 v84, v87
	v_exp_f32_e32 v44, v88
	v_exp_f32_e32 v45, v89
	v_exp_f32_e32 v46, v90
	v_exp_f32_e32 v47, v91
	v_exp_f32_e32 v48, v92
	v_exp_f32_e32 v49, v93
	v_exp_f32_e32 v50, v94
	v_exp_f32_e32 v51, v95
	v_exp_f32_e32 v75, v96
	v_exp_f32_e32 v85, v97
	v_exp_f32_e32 v86, v98
	v_exp_f32_e32 v87, v99
	v_exp_f32_e32 v88, v100
	v_exp_f32_e32 v89, v101
	v_exp_f32_e32 v90, v102
	v_exp_f32_e32 v91, v103
	v_mov_b32_e32 v72, 0
	v_mov_b32_e32 v76, 0
	v_mov_b32_e32 v73, 0
	v_mov_b32_e32 v77, 0
	v_cvt_pk_fp8_f32 v72, v36, v37
	v_cvt_pk_fp8_f32 v76, v44, v45
	v_cvt_pk_fp8_f32 v73, v40, v41
	v_cvt_pk_fp8_f32 v77, v48, v49
	v_cvt_pk_fp8_f32 v72, v38, v39 op_sel:[0,0,1]
	v_cvt_pk_fp8_f32 v76, v46, v47 op_sel:[0,0,1]
	v_cvt_pk_fp8_f32 v73, v42, v43 op_sel:[0,0,1]
	v_cvt_pk_fp8_f32 v77, v50, v51 op_sel:[0,0,1]
	v_mfma_f32_16x16x128_f8f6f4 v[200:203], v[124:131], v[148:155], v[200:203]
	v_mov_b32_e32 v78, 0
	v_mov_b32_e32 v79, 0
	v_mov_b32_e32 v74, 0
	v_cvt_pk_fp8_f32 v78, v75, v85
	v_mov_b32_e32 v75, 0
	v_cvt_pk_fp8_f32 v74, v53, v54
	v_cvt_pk_fp8_f32 v75, v81, v82
	v_cvt_pk_fp8_f32 v79, v88, v89
	v_cvt_pk_fp8_f32 v78, v86, v87 op_sel:[0,0,1]
	v_cvt_pk_fp8_f32 v74, v55, v80 op_sel:[0,0,1]
	v_cvt_pk_fp8_f32 v75, v83, v84 op_sel:[0,0,1]
	v_cvt_pk_fp8_f32 v79, v90, v91 op_sel:[0,0,1]
	ds_read_b128 v[80:83], v113 offset:16384
	s_nop 1
	ds_read_b128 v[58:61], v113 offset:16896
	ds_read_b128 v[84:87], v113 offset:17408
	ds_read_b128 v[62:65], v113 offset:17920
	s_mov_b32 s12, 0x43c80000
	v_mfma_f32_16x16x128_f8f6f4 v[200:203], v[124:131], v[72:79], v[200:203]
	s_nop 15
	s_nop 3
	v_sub_f32_e32 v37, v200, v204
	v_max3_f32 v0, v0, v52, v37
	v_cmp_nge_f32_e32 vcc, s12, v0
	s_cmp_lg_u64 vcc, 0
	s_cselect_b64 s[12:13], -1, 0
	s_cbranch_vccz .LBB1_12
	v_mfma_f32_32x32x64_f8f6f4 v[4:19], v[104:111], v[132:139], v[4:19]
	s_andn2_b64 vcc, exec, s[12:13]
	v_mfma_f32_32x32x64_f8f6f4 v[20:35], v[140:147], v[132:139], v[20:35]
	s_cbranch_vccnz .LBB1_5

.LBB1_5:
	s_waitcnt lgkmcnt(6)
	v_mfma_f32_32x32x64_f8f6f4 v[4:19], v[156:163], v[148:155], v[4:19]
	v_cmp_eq_u32_e32 vcc, 0, v1
	s_nop 1
	s_and_saveexec_b64 s[0:1], vcc
	s_lshl_b32 s12, s29, 2
	s_add_i32 s12, s12, 0x12000
	v_mov_b32_e32 v1, s12
	ds_write_b32 v1, v0
	s_or_b64 exec, exec, s[0:1]
	s_waitcnt vmcnt(0) lgkmcnt(0)
	s_barrier
	s_waitcnt lgkmcnt(4)
	v_mfma_f32_32x32x64_f8f6f4 v[20:35], v[164:171], v[148:155], v[20:35]
	s_waitcnt lgkmcnt(1)
	v_mfma_f32_32x32x64_f8f6f4 v[4:19], v[80:87], v[72:79], v[4:19]
	v_mov_b32_e32 v104, 0x12000
	ds_read_b128 v[38:41], v104
	ds_read_b128 v[42:45], v104 offset:16
	s_mov_b32 s14, 0
	s_waitcnt lgkmcnt(0)
	v_or_b32_e32 v0, v39, v38
	v_or_b32_e32 v0, v40, v0
	v_or_b32_e32 v0, v41, v0
	v_or_b32_e32 v0, v42, v0
	v_or_b32_e32 v0, v43, v0
	v_or_b32_e32 v0, v44, v0
	v_or_b32_e32 v0, v45, v0
	v_mfma_f32_32x32x64_f8f6f4 v[20:35], v[58:65], v[72:79], v[20:35]
	v_cmp_ne_u32_e32 vcc, 0, v0
	s_cbranch_vccnz .LBB1_13
	s_mov_b64 s[0:1], -1
	v_mov_b32_e32 v54, v4
	s_nop 15
	v_mov_b32_e32 v38, v20
	v_mov_b32_e32 v55, v5
	v_mov_b32_e32 v39, v21
	v_mov_b32_e32 v56, v6
	v_mov_b32_e32 v40, v22
	v_mov_b32_e32 v57, v7
	v_mov_b32_e32 v41, v23
	v_mov_b32_e32 v58, v8
	v_mov_b32_e32 v42, v24
	v_mov_b32_e32 v59, v9
	v_mov_b32_e32 v43, v25
	v_mov_b32_e32 v60, v10
	v_mov_b32_e32 v44, v26
	v_mov_b32_e32 v61, v11
	v_mov_b32_e32 v45, v27
	v_mov_b32_e32 v62, v12
	v_mov_b32_e32 v46, v28
	v_mov_b32_e32 v63, v13
	v_mov_b32_e32 v47, v29
	v_mov_b32_e32 v64, v14
	v_mov_b32_e32 v48, v30
	v_mov_b32_e32 v65, v15
	v_mov_b32_e32 v49, v31
	v_mov_b32_e32 v66, v16
	v_mov_b32_e32 v50, v32
	v_mov_b32_e32 v67, v17
	v_mov_b32_e32 v51, v33
	v_mov_b32_e32 v68, v18
	v_mov_b32_e32 v52, v34
	v_mov_b32_e32 v69, v19
	v_mov_b32_e32 v53, v35
.LBB1_9:
	v_mov_b64_e32 v[100:101], v[68:69]
	s_nop 8
	v_mov_b64_e32 v[84:85], v[52:53]
	s_and_b64 vcc, exec, s[0:1]
	v_mov_b64_e32 v[98:99], v[66:67]
	v_mov_b64_e32 v[96:97], v[64:65]
	v_mov_b64_e32 v[94:95], v[62:63]
	v_mov_b64_e32 v[92:93], v[60:61]
	v_mov_b64_e32 v[90:91], v[58:59]
	v_mov_b64_e32 v[88:89], v[56:57]
	v_mov_b64_e32 v[86:87], v[54:55]
	v_mov_b64_e32 v[82:83], v[50:51]
	v_mov_b64_e32 v[80:81], v[48:49]
	v_mov_b64_e32 v[78:79], v[46:47]
	v_mov_b64_e32 v[76:77], v[44:45]
	v_mov_b64_e32 v[74:75], v[42:43]
	v_mov_b64_e32 v[72:73], v[40:41]
	v_mov_b64_e32 v[70:71], v[38:39]
	s_cbranch_vccz .LBB1_11
	v_mov_b64_e32 v[100:101], v[18:19]
	v_mov_b64_e32 v[84:85], v[34:35]
	v_mul_f32_e32 v141, 0.5, v200
	v_mov_b64_e32 v[98:99], v[16:17]
	v_mov_b64_e32 v[96:97], v[14:15]
	v_mov_b64_e32 v[94:95], v[12:13]
	v_mov_b64_e32 v[92:93], v[10:11]
	v_mov_b64_e32 v[90:91], v[8:9]
	v_mov_b64_e32 v[88:89], v[6:7]
	v_mov_b64_e32 v[86:87], v[4:5]
	v_mov_b64_e32 v[82:83], v[32:33]
	v_mov_b64_e32 v[80:81], v[30:31]
	v_mov_b64_e32 v[78:79], v[28:29]
	v_mov_b64_e32 v[76:77], v[26:27]
	v_mov_b64_e32 v[74:75], v[24:25]
	v_mov_b64_e32 v[72:73], v[22:23]
	v_mov_b64_e32 v[70:71], v[20:21]
	v_mov_b32_e32 v146, v3

.LBB1_12:
	s_cmp_lg_u64 s[0:1], 0
	s_cselect_b64 s[0:1], -1, 0
	v_cndmask_b32_e64 v0, 0, 1, s[0:1]
	s_mov_b32 s0, 0x7f61b1e6
	v_cmp_nge_f32_e32 vcc, s0, v200
	s_cmp_lg_u64 vcc, 0
	s_cselect_b64 s[12:13], -1, 0
	v_mfma_f32_32x32x64_f8f6f4 v[4:19], v[104:111], v[132:139], v[4:19]
	s_andn2_b64 vcc, exec, s[12:13]
	v_mfma_f32_32x32x64_f8f6f4 v[20:35], v[140:147], v[132:139], v[20:35]
	s_cbranch_vccz .LBB1_4
	s_branch .LBB1_5

.LBB1_15:
	v_add_u32_e32 v105, s0, v176
	ds_read_b128 v[74:77], v105 offset:1024
	ds_read_b128 v[70:73], v105
	ds_read_b128 v[86:89], v105 offset:512
	ds_read_b128 v[90:93], v105 offset:1536
	s_cmp_eq_u32 s14, 0
	s_cselect_b64 s[0:1], -1, 0
	s_waitcnt lgkmcnt(2)
	v_mfma_f32_32x32x64_f8f6f4 v[70:85], v[70:77], v[116:123], 0
	s_mov_b64 s[12:13], -1
	s_and_b64 vcc, exec, s[0:1]
	s_nop 15
	s_nop 1
	v_max_f32_e32 v94, v71, v71
	v_max_f32_e32 v95, v70, v70
	v_max_f32_e32 v146, v95, v94
	s_waitcnt lgkmcnt(0)
	v_mfma_f32_32x32x64_f8f6f4 v[86:101], v[86:93], v[116:123], 0
	s_nop 15
	s_nop 3
	v_max3_f32 v147, v72, v73, v87
	v_max3_f32 v146, v146, v86, v88
	v_max3_f32 v146, v146, v89, v74
	v_max3_f32 v147, v147, v76, v77
	v_max3_f32 v146, v146, v75, v90
	v_max3_f32 v147, v147, v92, v93
	v_max3_f32 v147, v147, v80, v81
	v_max3_f32 v146, v146, v91, v78
	v_max3_f32 v147, v147, v96, v97
	v_max3_f32 v146, v146, v79, v94
	v_max3_f32 v147, v147, v84, v85
	v_max3_f32 v146, v146, v95, v82
	v_max3_f32 v147, v147, v100, v101
	v_max3_f32 v146, v146, v83, v98
	v_max3_f32 v146, v146, v99, v147
	v_mov_b32_e32 v147, v146
	s_nop 1
	v_permlane32_swap_b32_e32 v146, v147
	v_max_f32_e32 v147, v147, v147
	v_max_f32_e32 v146, v146, v146
	v_max_f32_e32 v146, v146, v147
	v_add_f32_e32 v146, v2, v146
	s_cbranch_vccnz .LBB1_19
	v_sub_f32_e32 v147, v146, v104
	v_cmp_lt_f32_e32 vcc, 2.0, v147
	s_cbranch_vccz .LBB1_18
	v_max_f32_e32 v146, v146, v146
	v_max_f32_e32 v147, v104, v104
	v_max_f32_e32 v146, v147, v146
	s_branch .LBB1_19

.LBB1_21:
	v_sub_f32_e32 v104, v2, v146
	v_add_f32_e32 v104, 0x40c00000, v104
	v_add_f32_e32 v70, v104, v70
	v_exp_f32_e32 v107, v70
	v_add_f32_e32 v70, v104, v86
	v_exp_f32_e32 v106, v70
	v_add_f32_e32 v70, v104, v71
	v_exp_f32_e32 v109, v70
	v_add_f32_e32 v70, v104, v87
	v_exp_f32_e32 v108, v70
	v_add_f32_e32 v70, v104, v72
	v_exp_f32_e32 v111, v70
	v_add_f32_e32 v70, v104, v88
	v_exp_f32_e32 v110, v70
	v_add_f32_e32 v70, v104, v73
	v_exp_f32_e32 v113, v70
	v_add_f32_e32 v70, v104, v89
	v_exp_f32_e32 v112, v70
	v_add_f32_e32 v70, v104, v74
	v_exp_f32_e32 v115, v70
	v_add_f32_e32 v70, v104, v90
	v_exp_f32_e32 v114, v70
	v_add_f32_e32 v70, v104, v75
	v_exp_f32_e32 v125, v70
	v_add_f32_e32 v70, v104, v91
	v_exp_f32_e32 v124, v70
	v_add_f32_e32 v70, v104, v76
	v_exp_f32_e32 v127, v70
	v_add_f32_e32 v70, v104, v92
	v_exp_f32_e32 v126, v70
	v_add_f32_e32 v70, v104, v77
	v_exp_f32_e32 v129, v70
	v_add_f32_e32 v70, v104, v93
	v_exp_f32_e32 v128, v70
	v_add_f32_e32 v70, v104, v78
	v_exp_f32_e32 v131, v70
	v_add_f32_e32 v70, v104, v94
	v_exp_f32_e32 v130, v70
	v_add_f32_e32 v70, v104, v79
	v_exp_f32_e32 v133, v70
	v_add_f32_e32 v70, v104, v95
	v_exp_f32_e32 v132, v70
	v_add_f32_e32 v70, v104, v80
	v_exp_f32_e32 v95, v70
	v_add_f32_e32 v70, v104, v96
	v_exp_f32_e32 v94, v70
	v_add_f32_e32 v70, v104, v81
	v_exp_f32_e32 v135, v70
	v_add_f32_e32 v70, v104, v97
	v_exp_f32_e32 v134, v70
	v_add_f32_e32 v70, v104, v82
	v_exp_f32_e32 v97, v70
	v_add_f32_e32 v70, v104, v98
	v_exp_f32_e32 v96, v70
	v_add_f32_e32 v70, v104, v83
	v_exp_f32_e32 v137, v70
	v_add_f32_e32 v70, v104, v99
	v_exp_f32_e32 v136, v70
	v_add_f32_e32 v70, v104, v84
	v_exp_f32_e32 v99, v70
	v_add_f32_e32 v70, v104, v100
	v_exp_f32_e32 v98, v70
	v_add_f32_e32 v70, v104, v85
	v_exp_f32_e32 v139, v70
	v_add_f32_e32 v70, v104, v101
	v_exp_f32_e32 v138, v70
	v_mov_b32_e32 v70, 0
	v_mov_b32_e32 v74, 0
	v_mov_b32_e32 v71, 0
	v_mov_b32_e32 v75, 0
	v_mov_b32_e32 v72, 0
	v_mov_b32_e32 v76, 0
	v_mov_b32_e32 v73, 0
	v_mov_b32_e32 v77, 0
	v_cvt_pk_fp8_f32 v70, v107, v109
	v_cvt_pk_fp8_f32 v74, v106, v108
	v_cvt_pk_fp8_f32 v71, v115, v125
	v_cvt_pk_fp8_f32 v75, v114, v124
	v_cvt_pk_fp8_f32 v72, v131, v133
	v_cvt_pk_fp8_f32 v76, v130, v132
	v_cvt_pk_fp8_f32 v73, v97, v137
	v_cvt_pk_fp8_f32 v77, v96, v136
	ds_read_b128 v[78:81], v105 offset:49152
	ds_read_b128 v[82:85], v105 offset:50176
	ds_read_b128 v[86:89], v105 offset:49664
	ds_read_b128 v[90:93], v105 offset:50688
	v_cvt_pk_fp8_f32 v70, v111, v113 op_sel:[0,0,1]
	v_cvt_pk_fp8_f32 v74, v110, v112 op_sel:[0,0,1]
	v_cvt_pk_fp8_f32 v71, v127, v129 op_sel:[0,0,1]
	v_cvt_pk_fp8_f32 v75, v126, v128 op_sel:[0,0,1]
	v_cvt_pk_fp8_f32 v72, v95, v135 op_sel:[0,0,1]
	v_cvt_pk_fp8_f32 v76, v94, v134 op_sel:[0,0,1]
	v_cvt_pk_fp8_f32 v73, v99, v139 op_sel:[0,0,1]
	v_cvt_pk_fp8_f32 v77, v98, v138 op_sel:[0,0,1]
	v_pk_add_f32 v[100:101], v[106:107], v[102:103]
	v_pk_add_f32 v[0:1], v[0:1], v[108:109]
	s_waitcnt lgkmcnt(2)
	v_mfma_f32_32x32x64_f8f6f4 v[54:69], v[78:85], v[70:77], v[54:69]
	v_add_f32_e64 v78, v110, v100
	v_add_f32_e64 v79, v111, v101
	v_add_f32_e64 v0, v0, v112
	v_add_f32_e64 v1, v1, v113
	v_add_f32_e64 v78, v114, v78
	v_add_f32_e64 v79, v115, v79
	v_add_f32_e64 v0, v0, v124
	v_add_f32_e64 v1, v1, v125
	v_add_f32_e64 v78, v126, v78
	v_add_f32_e64 v79, v127, v79
	v_add_f32_e64 v0, v0, v128
	v_add_f32_e64 v1, v1, v129
	v_add_f32_e64 v78, v130, v78
	v_add_f32_e64 v79, v131, v79
	v_pk_add_f32 v[0:1], v[0:1], v[132:133]
	v_pk_add_f32 v[78:79], v[94:95], v[78:79]
	v_pk_add_f32 v[0:1], v[0:1], v[134:135]
	s_waitcnt vmcnt(0) lgkmcnt(0)
	s_barrier
	v_pk_add_f32 v[78:79], v[96:97], v[78:79]
	v_pk_add_f32 v[0:1], v[0:1], v[136:137]
	s_addk_i32 s14, 0x4000
	s_add_i32 s15, s15, 1
	s_waitcnt lgkmcnt(0)
	v_mfma_f32_32x32x64_f8f6f4 v[38:53], v[86:93], v[70:77], v[38:53]
	v_add_f32_e64 v102, v98, v78
	v_add_f32_e64 v103, v99, v79
	v_add_f32_e64 v0, v0, v138
	v_add_f32_e64 v1, v1, v139
	s_cmp_eq_u32 s14, 0x80000
	s_cbranch_scc1 .LBB1_23
	v_mov_b32_e32 v104, v146
	v_mov_b32_e32 v106, v54
	v_mov_b32_e32 v107, v55
	v_mov_b32_e32 v108, v56
	v_mov_b32_e32 v109, v57
	v_mov_b32_e32 v110, v58
	v_mov_b32_e32 v111, v59
	v_mov_b32_e32 v112, v60
	v_mov_b32_e32 v113, v61
	v_mov_b32_e32 v114, v62
	v_mov_b32_e32 v115, v63
	v_mov_b32_e32 v124, v64
	v_mov_b32_e32 v125, v65
	v_mov_b32_e32 v126, v66
	v_mov_b32_e32 v127, v67
	v_mov_b32_e32 v128, v68
	v_mov_b32_e32 v129, v69
	v_mov_b32_e32 v130, v38
	v_mov_b32_e32 v131, v39
	v_mov_b32_e32 v132, v40
	v_mov_b32_e32 v133, v41
	v_mov_b32_e32 v134, v42
	v_mov_b32_e32 v135, v43
	v_mov_b32_e32 v136, v44
	v_mov_b32_e32 v137, v45
	v_mov_b32_e32 v138, v46
	v_mov_b32_e32 v139, v47
	v_mov_b32_e32 v140, v48
	v_mov_b32_e32 v141, v49
	v_mov_b32_e32 v142, v50
	v_mov_b32_e32 v143, v51
	v_mov_b32_e32 v144, v52
	v_mov_b32_e32 v145, v53
	s_and_b32 s0, s14, 0x4000
	s_cmp_eq_u32 s14, 0x7c000
	s_cbranch_scc0 .LBB1_14
	s_branch .LBB1_15

	.amdhsa_kernel _Z11attn_kernelPKfS0_S0_PKcS2_PKDv4_jS0_S0_S0_S0_Pf
		.amdhsa_group_segment_fixed_size 0
		.amdhsa_private_segment_fixed_size 0
		.amdhsa_kernarg_size 88
		.amdhsa_user_sgpr_count 2
		.amdhsa_user_sgpr_dispatch_ptr 0
		.amdhsa_user_sgpr_queue_ptr 0
		.amdhsa_user_sgpr_kernarg_segment_ptr 1
		.amdhsa_user_sgpr_dispatch_id 0
		.amdhsa_user_sgpr_kernarg_preload_length 0
		.amdhsa_user_sgpr_kernarg_preload_offset 0
		.amdhsa_user_sgpr_private_segment_size 0
		.amdhsa_uses_dynamic_stack 0
		.amdhsa_enable_private_segment 0
		.amdhsa_system_sgpr_workgroup_id_x 1
		.amdhsa_system_sgpr_workgroup_id_y 0
		.amdhsa_system_sgpr_workgroup_id_z 0
		.amdhsa_system_sgpr_workgroup_info 0
		.amdhsa_system_vgpr_workitem_id 0
		.amdhsa_next_free_vgpr 208
		.amdhsa_next_free_sgpr 39
		.amdhsa_accum_offset 208
		.amdhsa_reserve_vcc 1
		.amdhsa_float_round_mode_32 0
		.amdhsa_float_round_mode_16_64 0
		.amdhsa_float_denorm_mode_32 3
		.amdhsa_float_denorm_mode_16_64 3
		.amdhsa_dx10_clamp 1
		.amdhsa_ieee_mode 1
		.amdhsa_fp16_overflow 0
		.amdhsa_tg_split 0
		.amdhsa_exception_fp_ieee_invalid_op 0
		.amdhsa_exception_fp_denorm_src 0
		.amdhsa_exception_fp_ieee_div_zero 0
		.amdhsa_exception_fp_ieee_overflow 0
		.amdhsa_exception_fp_ieee_underflow 0
		.amdhsa_exception_fp_ieee_inexact 0
		.amdhsa_exception_int_div_zero 0
	.end_amdhsa_kernel

amdhsa.kernels:
  - .agpr_count:     32
    .args:
      - .actual_access:  read_only
        .address_space:  global
        .offset:         0
        .size:           8
        .value_kind:     global_buffer
      - .actual_access:  read_only
        .address_space:  global
        .offset:         8
        .size:           8
        .value_kind:     global_buffer
      - .actual_access:  read_only
        .address_space:  global
        .offset:         16
        .size:           8
        .value_kind:     global_buffer
      - .actual_access:  read_only
        .address_space:  global
        .offset:         24
        .size:           8
        .value_kind:     global_buffer
      - .actual_access:  read_only
        .address_space:  global
        .offset:         32
        .size:           8
        .value_kind:     global_buffer
      - .actual_access:  read_only
        .address_space:  global
        .offset:         40
        .size:           8
        .value_kind:     global_buffer
      - .actual_access:  read_only
        .address_space:  global
        .offset:         48
        .size:           8
        .value_kind:     global_buffer
      - .actual_access:  write_only
        .address_space:  global
        .offset:         56
        .size:           8
        .value_kind:     global_buffer
      - .actual_access:  write_only
        .address_space:  global
        .offset:         64
        .size:           8
        .value_kind:     global_buffer
      - .actual_access:  write_only
        .address_space:  global
        .offset:         72
        .size:           8
        .value_kind:     global_buffer
      - .actual_access:  write_only
        .address_space:  global
        .offset:         80
        .size:           8
        .value_kind:     global_buffer
      - .actual_access:  write_only
        .address_space:  global
        .offset:         88
        .size:           8
        .value_kind:     global_buffer
      - .actual_access:  write_only
        .address_space:  global
        .offset:         96
        .size:           8
        .value_kind:     global_buffer
      - .actual_access:  write_only
        .address_space:  global
        .offset:         104
        .size:           8
        .value_kind:     global_buffer
    .group_segment_fixed_size: 18944
    .kernarg_segment_align: 8
    .kernarg_segment_size: 112
    .language:       OpenCL C
    .language_version:
      - 2
      - 0
    .max_flat_workgroup_size: 256
    .name:           _Z11prep_kernelPKfS0_S0_S0_S0_S0_S0_PDv4_jS2_S2_PfS3_S3_S3_
    .private_segment_fixed_size: 0
    .sgpr_count:     24
    .sgpr_spill_count: 0
    .symbol:         _Z11prep_kernelPKfS0_S0_S0_S0_S0_S0_PDv4_jS2_S2_PfS3_S3_S3_.kd
    .uniform_work_group_size: 1
    .uses_dynamic_stack: false
    .vgpr_count:     132
    .vgpr_spill_count: 0
    .wavefront_size: 64
  - .agpr_count:     0
    .args:
      - .address_space:  global
        .offset:         0
        .size:           8
        .value_kind:     global_buffer
      - .address_space:  global
        .offset:         8
        .size:           8
        .value_kind:     global_buffer
      - .address_space:  global
        .offset:         16
        .size:           8
        .value_kind:     global_buffer
      - .address_space:  global
        .offset:         24
        .size:           8
        .value_kind:     global_buffer
      - .address_space:  global
        .offset:         32
        .size:           8
        .value_kind:     global_buffer
      - .actual_access:  read_only
        .address_space:  global
        .offset:         40
        .size:           8
        .value_kind:     global_buffer
      - .actual_access:  read_only
        .address_space:  global
        .offset:         48
        .size:           8
        .value_kind:     global_buffer
      - .address_space:  global
        .offset:         56
        .size:           8
        .value_kind:     global_buffer
      - .actual_access:  read_only
        .address_space:  global
        .offset:         64
        .size:           8
        .value_kind:     global_buffer
      - .actual_access:  read_only
        .address_space:  global
        .offset:         72
        .size:           8
        .value_kind:     global_buffer
      - .actual_access:  write_only
        .address_space:  global
        .offset:         80
        .size:           8
        .value_kind:     global_buffer
    .group_segment_fixed_size: 0
    .kernarg_segment_align: 8
    .kernarg_segment_size: 88
    .language:       OpenCL C
    .language_version:
      - 2
      - 0
    .max_flat_workgroup_size: 512
    .name:           _Z11attn_kernelPKfS0_S0_PKcS2_PKDv4_jS0_S0_S0_S0_Pf
    .private_segment_fixed_size: 0
    .sgpr_count:     45
    .sgpr_spill_count: 0
    .symbol:         _Z11attn_kernelPKfS0_S0_PKcS2_PKDv4_jS0_S0_S0_S0_Pf.kd
    .uniform_work_group_size: 1
    .uses_dynamic_stack: false
    .vgpr_count:     208
    .vgpr_spill_count: 0
    .wavefront_size: 64
